# v82 plus DPP wave reductions, in-proj epilogue scale loads hoisted, prologue GEMV double-buffered, dead movs removed
# speedup vs baseline: 1.0142x; 1.0142x over previous
; __device__ __forceinline__ void phase_prologue(const Params& p, const Ctx& F) {
;     ...
;         const int l = item / 96, cb = item % 96;
;         const float* W = p.w_ada + ((size_t)l * DM + F.wave * 256) * MODW + cb * 128 + 2 * F.lane;
;         float a0[9], a1[9];
; #pragma unroll
;         for (int r = 0; r < 9; ++r) { a0[r] = 0.f; a1[r] = 0.f; }
; #pragma unroll 8
;         for (int d = 0; d < 256; ++d) { const f32x2 w = *(const f32x2*)(W + (size_t)d * MODW);
; #pragma unroll
;             for (int r = 0; r < 9; ++r) { const float s = sl[r * DM + F.wave * 256 + d]; a0[r] += s * w.x; a1[r] += s * w.y; } }
.LBB0_12:
	s_or_b64 exec, exec, s[14:15]
	s_mul_hi_i32 s14, s30, 0x2aaaaaab
	s_lshr_b32 s15, s14, 31
	s_ashr_i32 s31, s14, 4
	s_add_i32 s31, s31, s15
	s_mul_i32 s14, s31, 0x60
	s_sub_i32 s14, s30, s14
	s_lshl_b32 s14, s14, 7
	s_ashr_i32 s15, s14, 31
	s_mul_i32 s35, s31, 0x6000000
	s_lshl_b64 s[16:17], s[14:15], 2
	s_mul_hi_i32 s34, s31, 0x6000000
	s_add_u32 s16, s35, s16
	s_addc_u32 s17, s34, s17
	v_mov_b32_e32 v14, 0
	v_lshl_add_u64 v[12:13], v[10:11], 0, s[16:17]
	s_mov_b32 s16, 0
	v_mov_b32_e32 v18, 0
	v_mov_b32_e32 v16, 0
	v_mov_b32_e32 v22, 0
	v_mov_b32_e32 v20, 0
	v_mov_b32_e32 v26, 0
	v_mov_b32_e32 v24, 0
	v_mov_b32_e32 v30, 0
	v_mov_b32_e32 v28, 0
	v_mov_b32_e32 v15, v14
	v_mov_b32_e32 v19, v14
	v_mov_b32_e32 v17, v14
	v_mov_b32_e32 v23, v14
	v_mov_b32_e32 v21, v14
	v_mov_b32_e32 v27, v14
	v_mov_b32_e32 v25, v14
	v_mov_b32_e32 v31, v14
	v_mov_b32_e32 v29, v14
	s_waitcnt lgkmcnt(0)
	s_barrier
	v_add_co_u32_e32 v32, vcc, s23, v12
	global_load_dwordx2 v[108:109], v[12:13], off
	s_nop 0
	v_addc_co_u32_e32 v33, vcc, -1, v13, vcc
	v_add_co_u32_e32 v34, vcc, s24, v12
	s_add_i32 s17, s19, s16
	s_nop 0
	v_addc_co_u32_e32 v35, vcc, -1, v13, vcc
	v_add_co_u32_e32 v36, vcc, s25, v12
	v_mov_b32_e32 v4, s17
	s_nop 0
	v_addc_co_u32_e32 v37, vcc, -1, v13, vcc
	v_add_co_u32_e32 v38, vcc, s26, v12
	s_add_i32 s34, s17, 0x10000
	s_nop 0
	v_addc_co_u32_e32 v39, vcc, -1, v13, vcc
	v_add_co_u32_e32 v44, vcc, s20, v12
	global_load_dwordx2 v[110:111], v[32:33], off
	global_load_dwordx2 v[112:113], v[34:35], off
	global_load_dwordx2 v[114:115], v[36:37], off
	global_load_dwordx2 v[116:117], v[38:39], off
	v_addc_co_u32_e32 v45, vcc, 0, v13, vcc
	v_add_co_u32_e32 v46, vcc, s27, v12
	s_add_i32 s17, s17, 0x10010
	s_nop 0
	v_addc_co_u32_e32 v47, vcc, 0, v13, vcc
	v_add_co_u32_e32 v48, vcc, s28, v12
	v_mov_b32_e32 v104, s17
	s_nop 0
	v_addc_co_u32_e32 v49, vcc, 0, v13, vcc
	global_load_dwordx2 v[118:119], v[44:45], off
	global_load_dwordx2 v[120:121], v[46:47], off
	global_load_dwordx2 v[122:123], v[48:49], off
.LBB0_13:
	v_lshl_add_u64 v[12:13], v[12:13], 0, s[12:13]
	v_add_co_u32_e32 v32, vcc, s23, v12
	global_load_dwordx2 v[158:159], v[12:13], off
	s_nop 0
	v_addc_co_u32_e32 v33, vcc, -1, v13, vcc
	v_add_co_u32_e32 v34, vcc, s24, v12
	s_add_i32 s17, s19, s16
	s_nop 0
	v_addc_co_u32_e32 v35, vcc, -1, v13, vcc
	v_add_co_u32_e32 v36, vcc, s25, v12
	v_mov_b32_e32 v4, s17
	s_nop 0
	v_addc_co_u32_e32 v37, vcc, -1, v13, vcc
	v_add_co_u32_e32 v38, vcc, s26, v12
	s_add_i32 s34, s17, 0x10000
	s_nop 0
	v_addc_co_u32_e32 v39, vcc, -1, v13, vcc
	v_add_co_u32_e32 v44, vcc, s20, v12
	global_load_dwordx2 v[160:161], v[32:33], off
	global_load_dwordx2 v[162:163], v[34:35], off
	global_load_dwordx2 v[164:165], v[36:37], off
	global_load_dwordx2 v[166:167], v[38:39], off
	v_addc_co_u32_e32 v45, vcc, 0, v13, vcc
	v_add_co_u32_e32 v46, vcc, s27, v12
	s_add_i32 s17, s17, 0x10010
	s_nop 0
	v_addc_co_u32_e32 v47, vcc, 0, v13, vcc
	v_add_co_u32_e32 v48, vcc, s28, v12
	v_mov_b32_e32 v104, s17
	s_nop 0
	v_addc_co_u32_e32 v49, vcc, 0, v13, vcc
	global_load_dwordx2 v[168:169], v[44:45], off
	global_load_dwordx2 v[170:171], v[46:47], off
	global_load_dwordx2 v[172:173], v[48:49], off
	ds_read_b128 v[32:35], v4
	ds_read_b128 v[36:39], v4 offset:16
	ds_read_b128 v[44:47], v4 offset:8192
	ds_read_b128 v[48:51], v4 offset:8208
	ds_read_b128 v[52:55], v4 offset:16384
	ds_read_b128 v[56:59], v4 offset:16400
	ds_read_b128 v[60:63], v4 offset:24576
	ds_read_b128 v[64:67], v4 offset:24592
	ds_read_b128 v[68:71], v4 offset:32768
	ds_read_b128 v[72:75], v4 offset:32784
	ds_read_b128 v[76:79], v4 offset:40960
	ds_read_b128 v[80:83], v4 offset:40976
	ds_read_b128 v[84:87], v4 offset:49152
	ds_read_b128 v[88:91], v4 offset:49168
	ds_read_b128 v[92:95], v4 offset:57344
	ds_read_b128 v[96:99], v4 offset:57360
	v_mov_b32_e32 v4, s34
	ds_read_b128 v[100:103], v4
	ds_read_b128 v[104:107], v104
	s_waitcnt lgkmcnt(14)
	v_mov_b32_e32 v4, v35
	v_mov_b32_e32 v124, v47
	s_waitcnt lgkmcnt(13)
	v_mov_b32_e32 v126, v55
	s_waitcnt lgkmcnt(11)
	v_mov_b32_e32 v128, v63
	s_waitcnt lgkmcnt(9)
	v_mov_b32_e32 v130, v71
	s_waitcnt lgkmcnt(7)
	v_mov_b32_e32 v132, v79
	s_waitcnt lgkmcnt(5)
	v_mov_b32_e32 v134, v87
	s_waitcnt lgkmcnt(3)
	v_mov_b32_e32 v136, v95
	s_waitcnt lgkmcnt(1)
	v_mov_b32_e32 v154, v103
	s_add_i32 s16, s16, 32
	v_mov_b32_e32 v138, v39
	v_mov_b32_e32 v140, v51
	v_mov_b32_e32 v142, v59
	v_mov_b32_e32 v144, v67
	v_mov_b32_e32 v146, v75
	v_mov_b32_e32 v148, v83
	v_mov_b32_e32 v150, v91
	v_mov_b32_e32 v152, v99
	s_waitcnt lgkmcnt(0)
	v_mov_b32_e32 v156, v107
	s_waitcnt vmcnt(14)
	v_pk_fma_f32 v[14:15], v[110:111], v[32:33], v[14:15] op_sel_hi:[1,0,1]
	v_pk_fma_f32 v[18:19], v[110:111], v[44:45], v[18:19] op_sel_hi:[1,0,1]
	v_pk_fma_f32 v[16:17], v[110:111], v[52:53], v[16:17] op_sel_hi:[1,0,1]
	v_pk_fma_f32 v[22:23], v[110:111], v[60:61], v[22:23] op_sel_hi:[1,0,1]
	v_pk_fma_f32 v[20:21], v[110:111], v[68:69], v[20:21] op_sel_hi:[1,0,1]
	v_pk_fma_f32 v[26:27], v[110:111], v[76:77], v[26:27] op_sel_hi:[1,0,1]
	v_pk_fma_f32 v[24:25], v[110:111], v[84:85], v[24:25] op_sel_hi:[1,0,1]
	v_pk_fma_f32 v[30:31], v[110:111], v[92:93], v[30:31] op_sel_hi:[1,0,1]
	v_pk_fma_f32 v[28:29], v[110:111], v[100:101], v[28:29] op_sel_hi:[1,0,1]
	s_waitcnt vmcnt(13)
	v_pk_fma_f32 v[14:15], v[112:113], v[32:33], v[14:15] op_sel:[0,1,0]
	v_pk_fma_f32 v[18:19], v[112:113], v[44:45], v[18:19] op_sel:[0,1,0]
	v_pk_fma_f32 v[16:17], v[112:113], v[52:53], v[16:17] op_sel:[0,1,0]
	v_pk_fma_f32 v[22:23], v[112:113], v[60:61], v[22:23] op_sel:[0,1,0]
	v_pk_fma_f32 v[20:21], v[112:113], v[68:69], v[20:21] op_sel:[0,1,0]
	v_pk_fma_f32 v[26:27], v[112:113], v[76:77], v[26:27] op_sel:[0,1,0]
	v_pk_fma_f32 v[24:25], v[112:113], v[84:85], v[24:25] op_sel:[0,1,0]
	v_pk_fma_f32 v[30:31], v[112:113], v[92:93], v[30:31] op_sel:[0,1,0]
	v_pk_fma_f32 v[28:29], v[112:113], v[100:101], v[28:29] op_sel:[0,1,0]
	s_waitcnt vmcnt(12)
; __device__ __forceinline__ void phase_prologue(const Params& p, const Ctx& F) {
;     ...
;         for (int d = 0; d < 256; ++d) { const f32x2 w = *(const f32x2*)(W + (size_t)d * MODW);
; #pragma unroll
;             for (int r = 0; r < 9; ++r) { const float s = sl[r * DM + F.wave * 256 + d]; a0[r] += s * w.x; a1[r] += s * w.y; } }
	v_pk_fma_f32 v[14:15], v[114:115], v[34:35], v[14:15] op_sel_hi:[1,0,1]
	v_pk_fma_f32 v[18:19], v[114:115], v[46:47], v[18:19] op_sel_hi:[1,0,1]
	v_pk_fma_f32 v[16:17], v[114:115], v[54:55], v[16:17] op_sel_hi:[1,0,1]
	v_pk_fma_f32 v[22:23], v[114:115], v[62:63], v[22:23] op_sel_hi:[1,0,1]
	v_pk_fma_f32 v[20:21], v[114:115], v[70:71], v[20:21] op_sel_hi:[1,0,1]
	v_pk_fma_f32 v[26:27], v[114:115], v[78:79], v[26:27] op_sel_hi:[1,0,1]
	v_pk_fma_f32 v[24:25], v[114:115], v[86:87], v[24:25] op_sel_hi:[1,0,1]
	v_pk_fma_f32 v[30:31], v[114:115], v[94:95], v[30:31] op_sel_hi:[1,0,1]
	v_pk_fma_f32 v[28:29], v[114:115], v[102:103], v[28:29] op_sel_hi:[1,0,1]
	s_waitcnt vmcnt(11)
	v_pk_fma_f32 v[14:15], v[116:117], v[4:5], v[14:15] op_sel_hi:[1,0,1]
	v_pk_fma_f32 v[18:19], v[116:117], v[124:125], v[18:19] op_sel_hi:[1,0,1]
	v_pk_fma_f32 v[16:17], v[116:117], v[126:127], v[16:17] op_sel_hi:[1,0,1]
	v_pk_fma_f32 v[22:23], v[116:117], v[128:129], v[22:23] op_sel_hi:[1,0,1]
	v_pk_fma_f32 v[20:21], v[116:117], v[130:131], v[20:21] op_sel_hi:[1,0,1]
	v_pk_fma_f32 v[26:27], v[116:117], v[132:133], v[26:27] op_sel_hi:[1,0,1]
	v_pk_fma_f32 v[24:25], v[116:117], v[134:135], v[24:25] op_sel_hi:[1,0,1]
	v_pk_fma_f32 v[30:31], v[116:117], v[136:137], v[30:31] op_sel_hi:[1,0,1]
	v_pk_fma_f32 v[28:29], v[116:117], v[154:155], v[28:29] op_sel_hi:[1,0,1]
	v_pk_fma_f32 v[14:15], v[108:109], v[36:37], v[14:15] op_sel_hi:[1,0,1]
	v_pk_fma_f32 v[18:19], v[108:109], v[48:49], v[18:19] op_sel_hi:[1,0,1]
	v_pk_fma_f32 v[16:17], v[108:109], v[56:57], v[16:17] op_sel_hi:[1,0,1]
	v_pk_fma_f32 v[22:23], v[108:109], v[64:65], v[22:23] op_sel_hi:[1,0,1]
	v_pk_fma_f32 v[20:21], v[108:109], v[72:73], v[20:21] op_sel_hi:[1,0,1]
	v_pk_fma_f32 v[26:27], v[108:109], v[80:81], v[26:27] op_sel_hi:[1,0,1]
	v_pk_fma_f32 v[24:25], v[108:109], v[88:89], v[24:25] op_sel_hi:[1,0,1]
	v_pk_fma_f32 v[30:31], v[108:109], v[96:97], v[30:31] op_sel_hi:[1,0,1]
	v_pk_fma_f32 v[28:29], v[108:109], v[104:105], v[28:29] op_sel_hi:[1,0,1]
	s_waitcnt vmcnt(10)
	v_pk_fma_f32 v[14:15], v[118:119], v[36:37], v[14:15] op_sel:[0,1,0]
	v_pk_fma_f32 v[18:19], v[118:119], v[48:49], v[18:19] op_sel:[0,1,0]
	v_pk_fma_f32 v[16:17], v[118:119], v[56:57], v[16:17] op_sel:[0,1,0]
	v_pk_fma_f32 v[22:23], v[118:119], v[64:65], v[22:23] op_sel:[0,1,0]
	v_pk_fma_f32 v[20:21], v[118:119], v[72:73], v[20:21] op_sel:[0,1,0]
	v_pk_fma_f32 v[26:27], v[118:119], v[80:81], v[26:27] op_sel:[0,1,0]
	v_pk_fma_f32 v[24:25], v[118:119], v[88:89], v[24:25] op_sel:[0,1,0]
	v_pk_fma_f32 v[30:31], v[118:119], v[96:97], v[30:31] op_sel:[0,1,0]
	v_pk_fma_f32 v[28:29], v[118:119], v[104:105], v[28:29] op_sel:[0,1,0]
	s_waitcnt vmcnt(9)
	v_pk_fma_f32 v[14:15], v[120:121], v[38:39], v[14:15] op_sel_hi:[1,0,1]
	v_pk_fma_f32 v[18:19], v[120:121], v[50:51], v[18:19] op_sel_hi:[1,0,1]
	v_pk_fma_f32 v[16:17], v[120:121], v[58:59], v[16:17] op_sel_hi:[1,0,1]
	v_pk_fma_f32 v[22:23], v[120:121], v[66:67], v[22:23] op_sel_hi:[1,0,1]
	v_pk_fma_f32 v[20:21], v[120:121], v[74:75], v[20:21] op_sel_hi:[1,0,1]
	v_pk_fma_f32 v[26:27], v[120:121], v[82:83], v[26:27] op_sel_hi:[1,0,1]
	v_pk_fma_f32 v[24:25], v[120:121], v[90:91], v[24:25] op_sel_hi:[1,0,1]
	v_pk_fma_f32 v[30:31], v[120:121], v[98:99], v[30:31] op_sel_hi:[1,0,1]
	v_pk_fma_f32 v[28:29], v[120:121], v[106:107], v[28:29] op_sel_hi:[1,0,1]
	s_waitcnt vmcnt(8)
	v_pk_fma_f32 v[14:15], v[122:123], v[138:139], v[14:15] op_sel_hi:[1,0,1]
	v_pk_fma_f32 v[18:19], v[122:123], v[140:141], v[18:19] op_sel_hi:[1,0,1]
	v_pk_fma_f32 v[16:17], v[122:123], v[142:143], v[16:17] op_sel_hi:[1,0,1]
	v_pk_fma_f32 v[22:23], v[122:123], v[144:145], v[22:23] op_sel_hi:[1,0,1]
	v_pk_fma_f32 v[20:21], v[122:123], v[146:147], v[20:21] op_sel_hi:[1,0,1]
	v_pk_fma_f32 v[26:27], v[122:123], v[148:149], v[26:27] op_sel_hi:[1,0,1]
	v_pk_fma_f32 v[24:25], v[122:123], v[150:151], v[24:25] op_sel_hi:[1,0,1]
	v_pk_fma_f32 v[30:31], v[122:123], v[152:153], v[30:31] op_sel_hi:[1,0,1]
	v_pk_fma_f32 v[28:29], v[122:123], v[156:157], v[28:29] op_sel_hi:[1,0,1]
	v_lshl_add_u64 v[12:13], v[12:13], 0, s[12:13]
	v_add_co_u32_e32 v32, vcc, s23, v12
	global_load_dwordx2 v[108:109], v[12:13], off
	s_nop 0
	v_addc_co_u32_e32 v33, vcc, -1, v13, vcc
	v_add_co_u32_e32 v34, vcc, s24, v12
	s_add_i32 s17, s19, s16
	s_nop 0
	v_addc_co_u32_e32 v35, vcc, -1, v13, vcc
	v_add_co_u32_e32 v36, vcc, s25, v12
	v_mov_b32_e32 v4, s17
	s_nop 0
	v_addc_co_u32_e32 v37, vcc, -1, v13, vcc
	v_add_co_u32_e32 v38, vcc, s26, v12
	s_add_i32 s34, s17, 0x10000
	s_nop 0
	v_addc_co_u32_e32 v39, vcc, -1, v13, vcc
	v_add_co_u32_e32 v44, vcc, s20, v12
	global_load_dwordx2 v[110:111], v[32:33], off
	global_load_dwordx2 v[112:113], v[34:35], off
	global_load_dwordx2 v[114:115], v[36:37], off
	global_load_dwordx2 v[116:117], v[38:39], off
	v_addc_co_u32_e32 v45, vcc, 0, v13, vcc
	v_add_co_u32_e32 v46, vcc, s27, v12
	s_add_i32 s17, s17, 0x10010
	s_nop 0
	v_addc_co_u32_e32 v47, vcc, 0, v13, vcc
	v_add_co_u32_e32 v48, vcc, s28, v12
	v_mov_b32_e32 v104, s17
	s_nop 0
	v_addc_co_u32_e32 v49, vcc, 0, v13, vcc
	global_load_dwordx2 v[118:119], v[44:45], off
	global_load_dwordx2 v[120:121], v[46:47], off
	global_load_dwordx2 v[122:123], v[48:49], off
	ds_read_b128 v[32:35], v4
	ds_read_b128 v[36:39], v4 offset:16
	ds_read_b128 v[44:47], v4 offset:8192
	ds_read_b128 v[48:51], v4 offset:8208
	ds_read_b128 v[52:55], v4 offset:16384
	ds_read_b128 v[56:59], v4 offset:16400
	ds_read_b128 v[60:63], v4 offset:24576
	ds_read_b128 v[64:67], v4 offset:24592
	ds_read_b128 v[68:71], v4 offset:32768
	ds_read_b128 v[72:75], v4 offset:32784
	ds_read_b128 v[76:79], v4 offset:40960
	ds_read_b128 v[80:83], v4 offset:40976
	ds_read_b128 v[84:87], v4 offset:49152
	ds_read_b128 v[88:91], v4 offset:49168
	ds_read_b128 v[92:95], v4 offset:57344
	ds_read_b128 v[96:99], v4 offset:57360
	v_mov_b32_e32 v4, s34
	ds_read_b128 v[100:103], v4
	ds_read_b128 v[104:107], v104
	s_waitcnt lgkmcnt(14)
; __device__ __forceinline__ void phase_prologue(const Params& p, const Ctx& F) {
;     ...
;         for (int d = 0; d < 256; ++d) { const f32x2 w = *(const f32x2*)(W + (size_t)d * MODW);
; #pragma unroll
;             for (int r = 0; r < 9; ++r) { const float s = sl[r * DM + F.wave * 256 + d]; a0[r] += s * w.x; a1[r] += s * w.y; } }
	v_mov_b32_e32 v4, v35
	v_mov_b32_e32 v124, v47
	s_waitcnt lgkmcnt(13)
	v_mov_b32_e32 v126, v55
	s_waitcnt lgkmcnt(11)
	v_mov_b32_e32 v128, v63
	s_waitcnt lgkmcnt(9)
	v_mov_b32_e32 v130, v71
	s_waitcnt lgkmcnt(7)
	v_mov_b32_e32 v132, v79
	s_waitcnt lgkmcnt(5)
	v_mov_b32_e32 v134, v87
	s_waitcnt lgkmcnt(3)
	v_mov_b32_e32 v136, v95
	s_waitcnt lgkmcnt(1)
	v_mov_b32_e32 v154, v103
	s_add_i32 s16, s16, 32
	v_mov_b32_e32 v138, v39
	v_mov_b32_e32 v140, v51
	v_mov_b32_e32 v142, v59
	v_mov_b32_e32 v144, v67
	v_mov_b32_e32 v146, v75
	v_mov_b32_e32 v148, v83
	v_mov_b32_e32 v150, v91
	v_mov_b32_e32 v152, v99
	s_waitcnt lgkmcnt(0)
	v_mov_b32_e32 v156, v107
	s_waitcnt vmcnt(14)
	v_pk_fma_f32 v[14:15], v[160:161], v[32:33], v[14:15] op_sel_hi:[1,0,1]
	v_pk_fma_f32 v[18:19], v[160:161], v[44:45], v[18:19] op_sel_hi:[1,0,1]
	v_pk_fma_f32 v[16:17], v[160:161], v[52:53], v[16:17] op_sel_hi:[1,0,1]
	v_pk_fma_f32 v[22:23], v[160:161], v[60:61], v[22:23] op_sel_hi:[1,0,1]
	v_pk_fma_f32 v[20:21], v[160:161], v[68:69], v[20:21] op_sel_hi:[1,0,1]
	v_pk_fma_f32 v[26:27], v[160:161], v[76:77], v[26:27] op_sel_hi:[1,0,1]
	v_pk_fma_f32 v[24:25], v[160:161], v[84:85], v[24:25] op_sel_hi:[1,0,1]
	v_pk_fma_f32 v[30:31], v[160:161], v[92:93], v[30:31] op_sel_hi:[1,0,1]
	v_pk_fma_f32 v[28:29], v[160:161], v[100:101], v[28:29] op_sel_hi:[1,0,1]
	s_waitcnt vmcnt(13)
	v_pk_fma_f32 v[14:15], v[162:163], v[32:33], v[14:15] op_sel:[0,1,0]
	v_pk_fma_f32 v[18:19], v[162:163], v[44:45], v[18:19] op_sel:[0,1,0]
	v_pk_fma_f32 v[16:17], v[162:163], v[52:53], v[16:17] op_sel:[0,1,0]
	v_pk_fma_f32 v[22:23], v[162:163], v[60:61], v[22:23] op_sel:[0,1,0]
	v_pk_fma_f32 v[20:21], v[162:163], v[68:69], v[20:21] op_sel:[0,1,0]
	v_pk_fma_f32 v[26:27], v[162:163], v[76:77], v[26:27] op_sel:[0,1,0]
	v_pk_fma_f32 v[24:25], v[162:163], v[84:85], v[24:25] op_sel:[0,1,0]
	v_pk_fma_f32 v[30:31], v[162:163], v[92:93], v[30:31] op_sel:[0,1,0]
	v_pk_fma_f32 v[28:29], v[162:163], v[100:101], v[28:29] op_sel:[0,1,0]
	s_waitcnt vmcnt(12)
	v_pk_fma_f32 v[14:15], v[164:165], v[34:35], v[14:15] op_sel_hi:[1,0,1]
	v_pk_fma_f32 v[18:19], v[164:165], v[46:47], v[18:19] op_sel_hi:[1,0,1]
	v_pk_fma_f32 v[16:17], v[164:165], v[54:55], v[16:17] op_sel_hi:[1,0,1]
	v_pk_fma_f32 v[22:23], v[164:165], v[62:63], v[22:23] op_sel_hi:[1,0,1]
	v_pk_fma_f32 v[20:21], v[164:165], v[70:71], v[20:21] op_sel_hi:[1,0,1]
	v_pk_fma_f32 v[26:27], v[164:165], v[78:79], v[26:27] op_sel_hi:[1,0,1]
	v_pk_fma_f32 v[24:25], v[164:165], v[86:87], v[24:25] op_sel_hi:[1,0,1]
	v_pk_fma_f32 v[30:31], v[164:165], v[94:95], v[30:31] op_sel_hi:[1,0,1]
	v_pk_fma_f32 v[28:29], v[164:165], v[102:103], v[28:29] op_sel_hi:[1,0,1]
	s_waitcnt vmcnt(11)
	v_pk_fma_f32 v[14:15], v[166:167], v[4:5], v[14:15] op_sel_hi:[1,0,1]
	v_pk_fma_f32 v[18:19], v[166:167], v[124:125], v[18:19] op_sel_hi:[1,0,1]
	v_pk_fma_f32 v[16:17], v[166:167], v[126:127], v[16:17] op_sel_hi:[1,0,1]
	v_pk_fma_f32 v[22:23], v[166:167], v[128:129], v[22:23] op_sel_hi:[1,0,1]
	v_pk_fma_f32 v[20:21], v[166:167], v[130:131], v[20:21] op_sel_hi:[1,0,1]
	v_pk_fma_f32 v[26:27], v[166:167], v[132:133], v[26:27] op_sel_hi:[1,0,1]
	v_pk_fma_f32 v[24:25], v[166:167], v[134:135], v[24:25] op_sel_hi:[1,0,1]
	v_pk_fma_f32 v[30:31], v[166:167], v[136:137], v[30:31] op_sel_hi:[1,0,1]
	v_pk_fma_f32 v[28:29], v[166:167], v[154:155], v[28:29] op_sel_hi:[1,0,1]
	v_pk_fma_f32 v[14:15], v[158:159], v[36:37], v[14:15] op_sel_hi:[1,0,1]
	v_pk_fma_f32 v[18:19], v[158:159], v[48:49], v[18:19] op_sel_hi:[1,0,1]
	v_pk_fma_f32 v[16:17], v[158:159], v[56:57], v[16:17] op_sel_hi:[1,0,1]
	v_pk_fma_f32 v[22:23], v[158:159], v[64:65], v[22:23] op_sel_hi:[1,0,1]
	v_pk_fma_f32 v[20:21], v[158:159], v[72:73], v[20:21] op_sel_hi:[1,0,1]
	v_pk_fma_f32 v[26:27], v[158:159], v[80:81], v[26:27] op_sel_hi:[1,0,1]
	v_pk_fma_f32 v[24:25], v[158:159], v[88:89], v[24:25] op_sel_hi:[1,0,1]
	v_pk_fma_f32 v[30:31], v[158:159], v[96:97], v[30:31] op_sel_hi:[1,0,1]
	v_pk_fma_f32 v[28:29], v[158:159], v[104:105], v[28:29] op_sel_hi:[1,0,1]
	s_waitcnt vmcnt(10)
	v_pk_fma_f32 v[14:15], v[168:169], v[36:37], v[14:15] op_sel:[0,1,0]
	v_pk_fma_f32 v[18:19], v[168:169], v[48:49], v[18:19] op_sel:[0,1,0]
	v_pk_fma_f32 v[16:17], v[168:169], v[56:57], v[16:17] op_sel:[0,1,0]
	v_pk_fma_f32 v[22:23], v[168:169], v[64:65], v[22:23] op_sel:[0,1,0]
	v_pk_fma_f32 v[20:21], v[168:169], v[72:73], v[20:21] op_sel:[0,1,0]
	v_pk_fma_f32 v[26:27], v[168:169], v[80:81], v[26:27] op_sel:[0,1,0]
	v_pk_fma_f32 v[24:25], v[168:169], v[88:89], v[24:25] op_sel:[0,1,0]
	v_pk_fma_f32 v[30:31], v[168:169], v[96:97], v[30:31] op_sel:[0,1,0]
	v_pk_fma_f32 v[28:29], v[168:169], v[104:105], v[28:29] op_sel:[0,1,0]
	s_waitcnt vmcnt(9)
	v_pk_fma_f32 v[14:15], v[170:171], v[38:39], v[14:15] op_sel_hi:[1,0,1]
	v_pk_fma_f32 v[18:19], v[170:171], v[50:51], v[18:19] op_sel_hi:[1,0,1]
	v_pk_fma_f32 v[16:17], v[170:171], v[58:59], v[16:17] op_sel_hi:[1,0,1]
	v_pk_fma_f32 v[22:23], v[170:171], v[66:67], v[22:23] op_sel_hi:[1,0,1]
	v_pk_fma_f32 v[20:21], v[170:171], v[74:75], v[20:21] op_sel_hi:[1,0,1]
	v_pk_fma_f32 v[26:27], v[170:171], v[82:83], v[26:27] op_sel_hi:[1,0,1]
	v_pk_fma_f32 v[24:25], v[170:171], v[90:91], v[24:25] op_sel_hi:[1,0,1]
	v_pk_fma_f32 v[30:31], v[170:171], v[98:99], v[30:31] op_sel_hi:[1,0,1]
	v_pk_fma_f32 v[28:29], v[170:171], v[106:107], v[28:29] op_sel_hi:[1,0,1]
	s_waitcnt vmcnt(8)
	v_pk_fma_f32 v[14:15], v[172:173], v[138:139], v[14:15] op_sel_hi:[1,0,1]
	v_pk_fma_f32 v[18:19], v[172:173], v[140:141], v[18:19] op_sel_hi:[1,0,1]
	v_pk_fma_f32 v[16:17], v[172:173], v[142:143], v[16:17] op_sel_hi:[1,0,1]
	v_pk_fma_f32 v[22:23], v[172:173], v[144:145], v[22:23] op_sel_hi:[1,0,1]
	v_pk_fma_f32 v[20:21], v[172:173], v[146:147], v[20:21] op_sel_hi:[1,0,1]
	v_pk_fma_f32 v[26:27], v[172:173], v[148:149], v[26:27] op_sel_hi:[1,0,1]
	v_pk_fma_f32 v[24:25], v[172:173], v[150:151], v[24:25] op_sel_hi:[1,0,1]
	v_pk_fma_f32 v[30:31], v[172:173], v[152:153], v[30:31] op_sel_hi:[1,0,1]
	v_pk_fma_f32 v[28:29], v[172:173], v[156:157], v[28:29] op_sel_hi:[1,0,1]
	s_cmpk_eq_i32 s16, 0x3c0
	s_cbranch_scc0 .LBB0_13
; __device__ __forceinline__ void phase_prologue(const Params& p, const Ctx& F) {
;     ...
;         for (int d = 0; d < 256; ++d) { const f32x2 w = *(const f32x2*)(W + (size_t)d * MODW);
; #pragma unroll
;             for (int r = 0; r < 9; ++r) { const float s = sl[r * DM + F.wave * 256 + d]; a0[r] += s * w.x; a1[r] += s * w.y; } }
	v_lshl_add_u64 v[12:13], v[12:13], 0, s[12:13]
	v_add_co_u32_e32 v32, vcc, s23, v12
	global_load_dwordx2 v[158:159], v[12:13], off
	s_nop 0
	v_addc_co_u32_e32 v33, vcc, -1, v13, vcc
	v_add_co_u32_e32 v34, vcc, s24, v12
	s_add_i32 s17, s19, s16
	s_nop 0
	v_addc_co_u32_e32 v35, vcc, -1, v13, vcc
	v_add_co_u32_e32 v36, vcc, s25, v12
	v_mov_b32_e32 v4, s17
	s_nop 0
	v_addc_co_u32_e32 v37, vcc, -1, v13, vcc
	v_add_co_u32_e32 v38, vcc, s26, v12
	s_add_i32 s34, s17, 0x10000
	s_nop 0
	v_addc_co_u32_e32 v39, vcc, -1, v13, vcc
	v_add_co_u32_e32 v44, vcc, s20, v12
	global_load_dwordx2 v[160:161], v[32:33], off
	global_load_dwordx2 v[162:163], v[34:35], off
	global_load_dwordx2 v[164:165], v[36:37], off
	global_load_dwordx2 v[166:167], v[38:39], off
	v_addc_co_u32_e32 v45, vcc, 0, v13, vcc
	v_add_co_u32_e32 v46, vcc, s27, v12
	s_add_i32 s17, s17, 0x10010
	s_nop 0
	v_addc_co_u32_e32 v47, vcc, 0, v13, vcc
	v_add_co_u32_e32 v48, vcc, s28, v12
	v_mov_b32_e32 v104, s17
	s_nop 0
	v_addc_co_u32_e32 v49, vcc, 0, v13, vcc
	global_load_dwordx2 v[168:169], v[44:45], off
	global_load_dwordx2 v[170:171], v[46:47], off
	global_load_dwordx2 v[172:173], v[48:49], off
	ds_read_b128 v[32:35], v4
	ds_read_b128 v[36:39], v4 offset:16
	ds_read_b128 v[44:47], v4 offset:8192
	ds_read_b128 v[48:51], v4 offset:8208
	ds_read_b128 v[52:55], v4 offset:16384
	ds_read_b128 v[56:59], v4 offset:16400
	ds_read_b128 v[60:63], v4 offset:24576
	ds_read_b128 v[64:67], v4 offset:24592
	ds_read_b128 v[68:71], v4 offset:32768
	ds_read_b128 v[72:75], v4 offset:32784
	ds_read_b128 v[76:79], v4 offset:40960
	ds_read_b128 v[80:83], v4 offset:40976
	ds_read_b128 v[84:87], v4 offset:49152
	ds_read_b128 v[88:91], v4 offset:49168
	ds_read_b128 v[92:95], v4 offset:57344
	ds_read_b128 v[96:99], v4 offset:57360
	v_mov_b32_e32 v4, s34
	ds_read_b128 v[100:103], v4
	ds_read_b128 v[104:107], v104
	s_waitcnt lgkmcnt(14)
	v_mov_b32_e32 v4, v35
	v_mov_b32_e32 v124, v47
	s_waitcnt lgkmcnt(13)
	v_mov_b32_e32 v126, v55
	s_waitcnt lgkmcnt(11)
	v_mov_b32_e32 v128, v63
	s_waitcnt lgkmcnt(9)
	v_mov_b32_e32 v130, v71
	s_waitcnt lgkmcnt(7)
	v_mov_b32_e32 v132, v79
	s_waitcnt lgkmcnt(5)
	v_mov_b32_e32 v134, v87
	s_waitcnt lgkmcnt(3)
	v_mov_b32_e32 v136, v95
	s_waitcnt lgkmcnt(1)
	v_mov_b32_e32 v154, v103
	s_add_i32 s16, s16, 32
	v_mov_b32_e32 v138, v39
	v_mov_b32_e32 v140, v51
	v_mov_b32_e32 v142, v59
	v_mov_b32_e32 v144, v67
	v_mov_b32_e32 v146, v75
	v_mov_b32_e32 v148, v83
	v_mov_b32_e32 v150, v91
	v_mov_b32_e32 v152, v99
	s_waitcnt lgkmcnt(0)
	v_mov_b32_e32 v156, v107
	s_waitcnt vmcnt(14)
	v_pk_fma_f32 v[14:15], v[110:111], v[32:33], v[14:15] op_sel_hi:[1,0,1]
	v_pk_fma_f32 v[18:19], v[110:111], v[44:45], v[18:19] op_sel_hi:[1,0,1]
	v_pk_fma_f32 v[16:17], v[110:111], v[52:53], v[16:17] op_sel_hi:[1,0,1]
	v_pk_fma_f32 v[22:23], v[110:111], v[60:61], v[22:23] op_sel_hi:[1,0,1]
	v_pk_fma_f32 v[20:21], v[110:111], v[68:69], v[20:21] op_sel_hi:[1,0,1]
	v_pk_fma_f32 v[26:27], v[110:111], v[76:77], v[26:27] op_sel_hi:[1,0,1]
	v_pk_fma_f32 v[24:25], v[110:111], v[84:85], v[24:25] op_sel_hi:[1,0,1]
	v_pk_fma_f32 v[30:31], v[110:111], v[92:93], v[30:31] op_sel_hi:[1,0,1]
	v_pk_fma_f32 v[28:29], v[110:111], v[100:101], v[28:29] op_sel_hi:[1,0,1]
	s_waitcnt vmcnt(13)
	v_pk_fma_f32 v[14:15], v[112:113], v[32:33], v[14:15] op_sel:[0,1,0]
	v_pk_fma_f32 v[18:19], v[112:113], v[44:45], v[18:19] op_sel:[0,1,0]
	v_pk_fma_f32 v[16:17], v[112:113], v[52:53], v[16:17] op_sel:[0,1,0]
	v_pk_fma_f32 v[22:23], v[112:113], v[60:61], v[22:23] op_sel:[0,1,0]
	v_pk_fma_f32 v[20:21], v[112:113], v[68:69], v[20:21] op_sel:[0,1,0]
	v_pk_fma_f32 v[26:27], v[112:113], v[76:77], v[26:27] op_sel:[0,1,0]
	v_pk_fma_f32 v[24:25], v[112:113], v[84:85], v[24:25] op_sel:[0,1,0]
	v_pk_fma_f32 v[30:31], v[112:113], v[92:93], v[30:31] op_sel:[0,1,0]
	v_pk_fma_f32 v[28:29], v[112:113], v[100:101], v[28:29] op_sel:[0,1,0]
	s_waitcnt vmcnt(12)
	v_pk_fma_f32 v[14:15], v[114:115], v[34:35], v[14:15] op_sel_hi:[1,0,1]
	v_pk_fma_f32 v[18:19], v[114:115], v[46:47], v[18:19] op_sel_hi:[1,0,1]
	v_pk_fma_f32 v[16:17], v[114:115], v[54:55], v[16:17] op_sel_hi:[1,0,1]
	v_pk_fma_f32 v[22:23], v[114:115], v[62:63], v[22:23] op_sel_hi:[1,0,1]
	v_pk_fma_f32 v[20:21], v[114:115], v[70:71], v[20:21] op_sel_hi:[1,0,1]
	v_pk_fma_f32 v[26:27], v[114:115], v[78:79], v[26:27] op_sel_hi:[1,0,1]
	v_pk_fma_f32 v[24:25], v[114:115], v[86:87], v[24:25] op_sel_hi:[1,0,1]
	v_pk_fma_f32 v[30:31], v[114:115], v[94:95], v[30:31] op_sel_hi:[1,0,1]
	v_pk_fma_f32 v[28:29], v[114:115], v[102:103], v[28:29] op_sel_hi:[1,0,1]
	s_waitcnt vmcnt(11)
	v_pk_fma_f32 v[14:15], v[116:117], v[4:5], v[14:15] op_sel_hi:[1,0,1]
	v_pk_fma_f32 v[18:19], v[116:117], v[124:125], v[18:19] op_sel_hi:[1,0,1]
	v_pk_fma_f32 v[16:17], v[116:117], v[126:127], v[16:17] op_sel_hi:[1,0,1]
	v_pk_fma_f32 v[22:23], v[116:117], v[128:129], v[22:23] op_sel_hi:[1,0,1]
	v_pk_fma_f32 v[20:21], v[116:117], v[130:131], v[20:21] op_sel_hi:[1,0,1]
	v_pk_fma_f32 v[26:27], v[116:117], v[132:133], v[26:27] op_sel_hi:[1,0,1]
	v_pk_fma_f32 v[24:25], v[116:117], v[134:135], v[24:25] op_sel_hi:[1,0,1]
	v_pk_fma_f32 v[30:31], v[116:117], v[136:137], v[30:31] op_sel_hi:[1,0,1]
	v_pk_fma_f32 v[28:29], v[116:117], v[154:155], v[28:29] op_sel_hi:[1,0,1]
	v_pk_fma_f32 v[14:15], v[108:109], v[36:37], v[14:15] op_sel_hi:[1,0,1]
	v_pk_fma_f32 v[18:19], v[108:109], v[48:49], v[18:19] op_sel_hi:[1,0,1]
	v_pk_fma_f32 v[16:17], v[108:109], v[56:57], v[16:17] op_sel_hi:[1,0,1]
	v_pk_fma_f32 v[22:23], v[108:109], v[64:65], v[22:23] op_sel_hi:[1,0,1]
	v_pk_fma_f32 v[20:21], v[108:109], v[72:73], v[20:21] op_sel_hi:[1,0,1]
	v_pk_fma_f32 v[26:27], v[108:109], v[80:81], v[26:27] op_sel_hi:[1,0,1]
	v_pk_fma_f32 v[24:25], v[108:109], v[88:89], v[24:25] op_sel_hi:[1,0,1]
	v_pk_fma_f32 v[30:31], v[108:109], v[96:97], v[30:31] op_sel_hi:[1,0,1]
	v_pk_fma_f32 v[28:29], v[108:109], v[104:105], v[28:29] op_sel_hi:[1,0,1]
	s_waitcnt vmcnt(10)
; __device__ __forceinline__ void phase_prologue(const Params& p, const Ctx& F) {
;     ...
; #pragma unroll 8
;         for (int d = 0; d < 256; ++d) { const f32x2 w = *(const f32x2*)(W + (size_t)d * MODW);
; #pragma unroll
;             for (int r = 0; r < 9; ++r) { const float s = sl[r * DM + F.wave * 256 + d]; a0[r] += s * w.x; a1[r] += s * w.y; } }
; #pragma unroll
;         for (int r = 0; r < 9; ++r) { red[(F.wave * 9 + r) * 128 + 2 * F.lane] = a0[r]; red[(F.wave * 9 + r) * 128 + 2 * F.lane + 1] = a1[r]; }
	v_pk_fma_f32 v[14:15], v[118:119], v[36:37], v[14:15] op_sel:[0,1,0]
	v_pk_fma_f32 v[18:19], v[118:119], v[48:49], v[18:19] op_sel:[0,1,0]
	v_pk_fma_f32 v[16:17], v[118:119], v[56:57], v[16:17] op_sel:[0,1,0]
	v_pk_fma_f32 v[22:23], v[118:119], v[64:65], v[22:23] op_sel:[0,1,0]
	v_pk_fma_f32 v[20:21], v[118:119], v[72:73], v[20:21] op_sel:[0,1,0]
	v_pk_fma_f32 v[26:27], v[118:119], v[80:81], v[26:27] op_sel:[0,1,0]
	v_pk_fma_f32 v[24:25], v[118:119], v[88:89], v[24:25] op_sel:[0,1,0]
	v_pk_fma_f32 v[30:31], v[118:119], v[96:97], v[30:31] op_sel:[0,1,0]
	v_pk_fma_f32 v[28:29], v[118:119], v[104:105], v[28:29] op_sel:[0,1,0]
	s_waitcnt vmcnt(9)
	v_pk_fma_f32 v[14:15], v[120:121], v[38:39], v[14:15] op_sel_hi:[1,0,1]
	v_pk_fma_f32 v[18:19], v[120:121], v[50:51], v[18:19] op_sel_hi:[1,0,1]
	v_pk_fma_f32 v[16:17], v[120:121], v[58:59], v[16:17] op_sel_hi:[1,0,1]
	v_pk_fma_f32 v[22:23], v[120:121], v[66:67], v[22:23] op_sel_hi:[1,0,1]
	v_pk_fma_f32 v[20:21], v[120:121], v[74:75], v[20:21] op_sel_hi:[1,0,1]
	v_pk_fma_f32 v[26:27], v[120:121], v[82:83], v[26:27] op_sel_hi:[1,0,1]
	v_pk_fma_f32 v[24:25], v[120:121], v[90:91], v[24:25] op_sel_hi:[1,0,1]
	v_pk_fma_f32 v[30:31], v[120:121], v[98:99], v[30:31] op_sel_hi:[1,0,1]
	v_pk_fma_f32 v[28:29], v[120:121], v[106:107], v[28:29] op_sel_hi:[1,0,1]
	s_waitcnt vmcnt(8)
	v_pk_fma_f32 v[14:15], v[122:123], v[138:139], v[14:15] op_sel_hi:[1,0,1]
	v_pk_fma_f32 v[18:19], v[122:123], v[140:141], v[18:19] op_sel_hi:[1,0,1]
	v_pk_fma_f32 v[16:17], v[122:123], v[142:143], v[16:17] op_sel_hi:[1,0,1]
	v_pk_fma_f32 v[22:23], v[122:123], v[144:145], v[22:23] op_sel_hi:[1,0,1]
	v_pk_fma_f32 v[20:21], v[122:123], v[146:147], v[20:21] op_sel_hi:[1,0,1]
	v_pk_fma_f32 v[26:27], v[122:123], v[148:149], v[26:27] op_sel_hi:[1,0,1]
	v_pk_fma_f32 v[24:25], v[122:123], v[150:151], v[24:25] op_sel_hi:[1,0,1]
	v_pk_fma_f32 v[30:31], v[122:123], v[152:153], v[30:31] op_sel_hi:[1,0,1]
	v_pk_fma_f32 v[28:29], v[122:123], v[156:157], v[28:29] op_sel_hi:[1,0,1]
	v_add_co_u32_e32 v32, vcc, s23, v12
	s_nop 0
	v_addc_co_u32_e32 v33, vcc, -1, v13, vcc
	v_add_co_u32_e32 v34, vcc, s24, v12
	s_add_i32 s17, s19, s16
	s_nop 0
	v_addc_co_u32_e32 v35, vcc, -1, v13, vcc
	v_add_co_u32_e32 v36, vcc, s25, v12
	v_mov_b32_e32 v4, s17
	s_nop 0
	v_addc_co_u32_e32 v37, vcc, -1, v13, vcc
	v_add_co_u32_e32 v38, vcc, s26, v12
	s_add_i32 s34, s17, 0x10000
	s_nop 0
	v_addc_co_u32_e32 v39, vcc, -1, v13, vcc
	v_add_co_u32_e32 v44, vcc, s20, v12
	v_addc_co_u32_e32 v45, vcc, 0, v13, vcc
	v_add_co_u32_e32 v46, vcc, s27, v12
	s_add_i32 s17, s17, 0x10010
	s_nop 0
	v_addc_co_u32_e32 v47, vcc, 0, v13, vcc
	v_add_co_u32_e32 v48, vcc, s28, v12
	v_mov_b32_e32 v104, s17
	s_nop 0
	v_addc_co_u32_e32 v49, vcc, 0, v13, vcc
	ds_read_b128 v[32:35], v4
	ds_read_b128 v[36:39], v4 offset:16
	ds_read_b128 v[44:47], v4 offset:8192
	ds_read_b128 v[48:51], v4 offset:8208
	ds_read_b128 v[52:55], v4 offset:16384
	ds_read_b128 v[56:59], v4 offset:16400
	ds_read_b128 v[60:63], v4 offset:24576
	ds_read_b128 v[64:67], v4 offset:24592
	ds_read_b128 v[68:71], v4 offset:32768
	ds_read_b128 v[72:75], v4 offset:32784
	ds_read_b128 v[76:79], v4 offset:40960
	ds_read_b128 v[80:83], v4 offset:40976
	ds_read_b128 v[84:87], v4 offset:49152
	ds_read_b128 v[88:91], v4 offset:49168
	ds_read_b128 v[92:95], v4 offset:57344
	ds_read_b128 v[96:99], v4 offset:57360
	v_mov_b32_e32 v4, s34
	ds_read_b128 v[100:103], v4
	ds_read_b128 v[104:107], v104
	s_waitcnt lgkmcnt(14)
	v_mov_b32_e32 v4, v35
	v_mov_b32_e32 v124, v47
	s_waitcnt lgkmcnt(13)
	v_mov_b32_e32 v126, v55
	s_waitcnt lgkmcnt(11)
	v_mov_b32_e32 v128, v63
	s_waitcnt lgkmcnt(9)
	v_mov_b32_e32 v130, v71
	s_waitcnt lgkmcnt(7)
	v_mov_b32_e32 v132, v79
	s_waitcnt lgkmcnt(5)
	v_mov_b32_e32 v134, v87
	s_waitcnt lgkmcnt(3)
	v_mov_b32_e32 v136, v95
	s_waitcnt lgkmcnt(1)
	v_mov_b32_e32 v154, v103
	s_add_i32 s16, s16, 32
	v_mov_b32_e32 v138, v39
	v_mov_b32_e32 v140, v51
	v_mov_b32_e32 v142, v59
	v_mov_b32_e32 v144, v67
	v_mov_b32_e32 v146, v75
	v_mov_b32_e32 v148, v83
	v_mov_b32_e32 v150, v91
	v_mov_b32_e32 v152, v99
	s_waitcnt lgkmcnt(0)
	v_mov_b32_e32 v156, v107
	s_waitcnt vmcnt(6)
	v_pk_fma_f32 v[14:15], v[160:161], v[32:33], v[14:15] op_sel_hi:[1,0,1]
	v_pk_fma_f32 v[18:19], v[160:161], v[44:45], v[18:19] op_sel_hi:[1,0,1]
	v_pk_fma_f32 v[16:17], v[160:161], v[52:53], v[16:17] op_sel_hi:[1,0,1]
	v_pk_fma_f32 v[22:23], v[160:161], v[60:61], v[22:23] op_sel_hi:[1,0,1]
	v_pk_fma_f32 v[20:21], v[160:161], v[68:69], v[20:21] op_sel_hi:[1,0,1]
	v_pk_fma_f32 v[26:27], v[160:161], v[76:77], v[26:27] op_sel_hi:[1,0,1]
	v_pk_fma_f32 v[24:25], v[160:161], v[84:85], v[24:25] op_sel_hi:[1,0,1]
	v_pk_fma_f32 v[30:31], v[160:161], v[92:93], v[30:31] op_sel_hi:[1,0,1]
	v_pk_fma_f32 v[28:29], v[160:161], v[100:101], v[28:29] op_sel_hi:[1,0,1]
	s_waitcnt vmcnt(5)
; __device__ __forceinline__ void phase_prologue(const Params& p, const Ctx& F) {
;     ...
;         for (int d = 0; d < 256; ++d) { const f32x2 w = *(const f32x2*)(W + (size_t)d * MODW);
; #pragma unroll
;             for (int r = 0; r < 9; ++r) { const float s = sl[r * DM + F.wave * 256 + d]; a0[r] += s * w.x; a1[r] += s * w.y; } }
; #pragma unroll
;         for (int r = 0; r < 9; ++r) { red[(F.wave * 9 + r) * 128 + 2 * F.lane] = a0[r]; red[(F.wave * 9 + r) * 128 + 2 * F.lane + 1] = a1[r]; }
;         __syncthreads();
;         for (int i = F.tid; i < 9 * 128; i += NTHR) { const int r = i >> 7, cc = i & 127; float s = p.b_ada[l * MODW + cb * 128 + cc];
; #pragma unroll
;             for (int w = 0; w < 8; ++w) s += red[(w * 9 + r) * 128 + cc];
;             F.mod[(size_t)(l * 9 + r) * MODW + cb * 128 + cc] = s; }
	v_pk_fma_f32 v[14:15], v[162:163], v[32:33], v[14:15] op_sel:[0,1,0]
	v_pk_fma_f32 v[18:19], v[162:163], v[44:45], v[18:19] op_sel:[0,1,0]
	v_pk_fma_f32 v[16:17], v[162:163], v[52:53], v[16:17] op_sel:[0,1,0]
	v_pk_fma_f32 v[22:23], v[162:163], v[60:61], v[22:23] op_sel:[0,1,0]
	v_pk_fma_f32 v[20:21], v[162:163], v[68:69], v[20:21] op_sel:[0,1,0]
	v_pk_fma_f32 v[26:27], v[162:163], v[76:77], v[26:27] op_sel:[0,1,0]
	v_pk_fma_f32 v[24:25], v[162:163], v[84:85], v[24:25] op_sel:[0,1,0]
	v_pk_fma_f32 v[30:31], v[162:163], v[92:93], v[30:31] op_sel:[0,1,0]
	v_pk_fma_f32 v[28:29], v[162:163], v[100:101], v[28:29] op_sel:[0,1,0]
	s_waitcnt vmcnt(4)
	v_pk_fma_f32 v[14:15], v[164:165], v[34:35], v[14:15] op_sel_hi:[1,0,1]
	v_pk_fma_f32 v[18:19], v[164:165], v[46:47], v[18:19] op_sel_hi:[1,0,1]
	v_pk_fma_f32 v[16:17], v[164:165], v[54:55], v[16:17] op_sel_hi:[1,0,1]
	v_pk_fma_f32 v[22:23], v[164:165], v[62:63], v[22:23] op_sel_hi:[1,0,1]
	v_pk_fma_f32 v[20:21], v[164:165], v[70:71], v[20:21] op_sel_hi:[1,0,1]
	v_pk_fma_f32 v[26:27], v[164:165], v[78:79], v[26:27] op_sel_hi:[1,0,1]
	v_pk_fma_f32 v[24:25], v[164:165], v[86:87], v[24:25] op_sel_hi:[1,0,1]
	v_pk_fma_f32 v[30:31], v[164:165], v[94:95], v[30:31] op_sel_hi:[1,0,1]
	v_pk_fma_f32 v[28:29], v[164:165], v[102:103], v[28:29] op_sel_hi:[1,0,1]
	s_waitcnt vmcnt(3)
	v_pk_fma_f32 v[14:15], v[166:167], v[4:5], v[14:15] op_sel_hi:[1,0,1]
	v_pk_fma_f32 v[18:19], v[166:167], v[124:125], v[18:19] op_sel_hi:[1,0,1]
	v_pk_fma_f32 v[16:17], v[166:167], v[126:127], v[16:17] op_sel_hi:[1,0,1]
	v_pk_fma_f32 v[22:23], v[166:167], v[128:129], v[22:23] op_sel_hi:[1,0,1]
	v_pk_fma_f32 v[20:21], v[166:167], v[130:131], v[20:21] op_sel_hi:[1,0,1]
	v_pk_fma_f32 v[26:27], v[166:167], v[132:133], v[26:27] op_sel_hi:[1,0,1]
	v_pk_fma_f32 v[24:25], v[166:167], v[134:135], v[24:25] op_sel_hi:[1,0,1]
	v_pk_fma_f32 v[30:31], v[166:167], v[136:137], v[30:31] op_sel_hi:[1,0,1]
	v_pk_fma_f32 v[28:29], v[166:167], v[154:155], v[28:29] op_sel_hi:[1,0,1]
	v_pk_fma_f32 v[14:15], v[158:159], v[36:37], v[14:15] op_sel_hi:[1,0,1]
	v_pk_fma_f32 v[18:19], v[158:159], v[48:49], v[18:19] op_sel_hi:[1,0,1]
	v_pk_fma_f32 v[16:17], v[158:159], v[56:57], v[16:17] op_sel_hi:[1,0,1]
	v_pk_fma_f32 v[22:23], v[158:159], v[64:65], v[22:23] op_sel_hi:[1,0,1]
	v_pk_fma_f32 v[20:21], v[158:159], v[72:73], v[20:21] op_sel_hi:[1,0,1]
	v_pk_fma_f32 v[26:27], v[158:159], v[80:81], v[26:27] op_sel_hi:[1,0,1]
	v_pk_fma_f32 v[24:25], v[158:159], v[88:89], v[24:25] op_sel_hi:[1,0,1]
	v_pk_fma_f32 v[30:31], v[158:159], v[96:97], v[30:31] op_sel_hi:[1,0,1]
	v_pk_fma_f32 v[28:29], v[158:159], v[104:105], v[28:29] op_sel_hi:[1,0,1]
	s_waitcnt vmcnt(2)
	v_pk_fma_f32 v[14:15], v[168:169], v[36:37], v[14:15] op_sel:[0,1,0]
	v_pk_fma_f32 v[18:19], v[168:169], v[48:49], v[18:19] op_sel:[0,1,0]
	v_pk_fma_f32 v[16:17], v[168:169], v[56:57], v[16:17] op_sel:[0,1,0]
	v_pk_fma_f32 v[22:23], v[168:169], v[64:65], v[22:23] op_sel:[0,1,0]
	v_pk_fma_f32 v[20:21], v[168:169], v[72:73], v[20:21] op_sel:[0,1,0]
	v_pk_fma_f32 v[26:27], v[168:169], v[80:81], v[26:27] op_sel:[0,1,0]
	v_pk_fma_f32 v[24:25], v[168:169], v[88:89], v[24:25] op_sel:[0,1,0]
	v_pk_fma_f32 v[30:31], v[168:169], v[96:97], v[30:31] op_sel:[0,1,0]
	v_pk_fma_f32 v[28:29], v[168:169], v[104:105], v[28:29] op_sel:[0,1,0]
	s_waitcnt vmcnt(1)
	v_pk_fma_f32 v[14:15], v[170:171], v[38:39], v[14:15] op_sel_hi:[1,0,1]
	v_pk_fma_f32 v[18:19], v[170:171], v[50:51], v[18:19] op_sel_hi:[1,0,1]
	v_pk_fma_f32 v[16:17], v[170:171], v[58:59], v[16:17] op_sel_hi:[1,0,1]
	v_pk_fma_f32 v[22:23], v[170:171], v[66:67], v[22:23] op_sel_hi:[1,0,1]
	v_pk_fma_f32 v[20:21], v[170:171], v[74:75], v[20:21] op_sel_hi:[1,0,1]
	v_pk_fma_f32 v[26:27], v[170:171], v[82:83], v[26:27] op_sel_hi:[1,0,1]
	v_pk_fma_f32 v[24:25], v[170:171], v[90:91], v[24:25] op_sel_hi:[1,0,1]
	v_pk_fma_f32 v[30:31], v[170:171], v[98:99], v[30:31] op_sel_hi:[1,0,1]
	v_pk_fma_f32 v[28:29], v[170:171], v[106:107], v[28:29] op_sel_hi:[1,0,1]
	s_waitcnt vmcnt(0)
	v_pk_fma_f32 v[14:15], v[172:173], v[138:139], v[14:15] op_sel_hi:[1,0,1]
	v_pk_fma_f32 v[18:19], v[172:173], v[140:141], v[18:19] op_sel_hi:[1,0,1]
	v_pk_fma_f32 v[16:17], v[172:173], v[142:143], v[16:17] op_sel_hi:[1,0,1]
	v_pk_fma_f32 v[22:23], v[172:173], v[144:145], v[22:23] op_sel_hi:[1,0,1]
	v_pk_fma_f32 v[20:21], v[172:173], v[146:147], v[20:21] op_sel_hi:[1,0,1]
	v_pk_fma_f32 v[26:27], v[172:173], v[148:149], v[26:27] op_sel_hi:[1,0,1]
	v_pk_fma_f32 v[24:25], v[172:173], v[150:151], v[24:25] op_sel_hi:[1,0,1]
	v_pk_fma_f32 v[30:31], v[172:173], v[152:153], v[30:31] op_sel_hi:[1,0,1]
	v_pk_fma_f32 v[28:29], v[172:173], v[156:157], v[28:29] op_sel_hi:[1,0,1]
	ds_write2st64_b64 v43, v[14:15], v[18:19] offset1:1
	ds_write2st64_b64 v43, v[16:17], v[22:23] offset0:2 offset1:3
	ds_write2st64_b64 v43, v[20:21], v[26:27] offset0:4 offset1:5
	ds_write2st64_b64 v43, v[24:25], v[30:31] offset0:6 offset1:7
	ds_write_b64 v43, v[28:29] offset:4096
	s_waitcnt lgkmcnt(0)
	s_barrier
	s_and_saveexec_b64 s[16:17], s[4:5]
	s_cbranch_execz .LBB0_8
	s_mul_i32 s34, s31, 0x3000
	s_add_i32 s34, s34, s14
	v_or_b32_e32 v12, s34, v40
	v_ashrrev_i32_e32 v13, 31, v12
	s_mul_i32 s31, s31, 9
	v_lshl_add_u64 v[12:13], v[12:13], 2, s[74:75]
	v_lshl_add_u64 v[14:15], s[14:15], 2, v[6:7]
	s_mov_b64 s[14:15], 0
	v_mov_b32_e32 v4, v2

; __device__ __forceinline__ float amax4(const f32x4& v) { return fmaxf(fmaxf(fabsf(v.x), fabsf(v.y)), fmaxf(fabsf(v.z), fabsf(v.w))); }
; __device__ __forceinline__ float wave_sum(float v) {
; #pragma unroll
;     for (int o = 1; o < 64; o <<= 1) v += __shfl_xor(v, o);
;     return v;
; __device__ __forceinline__ void phase_norm1(const Params& p, const Ctx& F, const int l) {
;     ...
;         float ss = 0.f;
; #pragma unroll
;         for (int j = 0; j < 8; ++j) ss += (v[j].x * v[j].x + v[j].y * v[j].y) + (v[j].z * v[j].z + v[j].w * v[j].w);
;         const float rstd = rsqrtf(wave_sum(ss) * (1.f / DM) + EPS);
;         if (fin) {
; #pragma unroll
;             for (int j = 0; j < 8; ++j) __builtin_nontemporal_store(v[j] * rstd * *((const f32x4*)p.g_final + F.lane + 64 * j), (f32x4*)xd + F.lane + 64 * j);
;         } else {
;             float am = 0.f;
; #pragma unroll
;             for (int j = 0; j < 8; ++j) { v[j] = v[j] * rstd * A[j] + Bv[j]; am = fmaxf(am, amax4(v[j])); }
.LBB0_174:
	v_mov_b32_e32 v200, v137
	v_mov_b32_e32 v201, v133
	v_mov_b32_e32 v198, v136
	v_mov_b32_e32 v199, v132
	v_pk_mul_f32 v[200:201], v[200:201], v[200:201]
	v_mov_b32_e32 v210, v139
	v_mov_b32_e32 v211, v135
	v_pk_fma_f32 v[198:199], v[198:199], v[198:199], v[200:201]
	v_mov_b32_e32 v200, v138
	v_mov_b32_e32 v201, v134
	v_pk_mul_f32 v[210:211], v[210:211], v[210:211]
	s_mov_b32 s12, 0x42fe0000
	v_pk_fma_f32 v[200:201], v[200:201], v[200:201], v[210:211]
	v_pk_mul_f32 v[210:211], v[140:141], v[140:141]
	v_pk_add_f32 v[198:199], v[198:199], v[200:201]
	v_pk_mul_f32 v[200:201], v[142:143], v[142:143]
	v_pk_add_f32 v[198:199], v[198:199], v[198:199] op_sel_hi:[0,1]
	v_pk_mov_b32 v[212:213], v[210:211], v[200:201] op_sel:[1,0]
	v_mov_b32_e32 v211, v201
	v_mul_f32_e32 v198, v144, v144
	v_pk_add_f32 v[200:201], v[212:213], v[210:211]
	v_pk_fma_f32 v[210:211], v[144:145], v[144:145], v[198:199] op_sel_hi:[1,1,0]
	v_mul_f32_e32 v198, v146, v146
	v_pk_add_f32 v[200:201], v[200:201], v[200:201] op_sel_hi:[0,1]
	v_pk_fma_f32 v[212:213], v[146:147], v[146:147], v[198:199] op_sel_hi:[1,1,0]
	v_mul_f32_e32 v210, v148, v148
	v_mul_f32_e32 v212, v149, v149
	v_mul_f32_e32 v200, v150, v150
	v_mul_f32_e32 v198, v151, v151
	v_pk_add_f32 v[210:211], v[210:211], v[212:213]
	v_pk_add_f32 v[198:199], v[200:201], v[198:199]
	v_pk_mul_f32 v[200:201], v[154:155], v[154:155]
	v_pk_add_f32 v[198:199], v[210:211], v[198:199]
	v_pk_mul_f32 v[210:211], v[152:153], v[152:153]
	v_pk_add_f32 v[198:199], v[198:199], v[198:199] op_sel_hi:[0,1]
	v_pk_mov_b32 v[212:213], v[210:211], v[200:201] op_sel:[1,0]
	v_mov_b32_e32 v211, v201
	v_mul_f32_e32 v198, v156, v156
	v_pk_add_f32 v[200:201], v[212:213], v[210:211]
	v_pk_fma_f32 v[210:211], v[156:157], v[156:157], v[198:199] op_sel_hi:[1,1,0]
	v_mul_f32_e32 v198, v158, v158
	v_pk_add_f32 v[200:201], v[200:201], v[200:201] op_sel_hi:[0,1]
	v_pk_fma_f32 v[212:213], v[158:159], v[158:159], v[198:199] op_sel_hi:[1,1,0]
	v_mul_f32_e32 v210, v160, v160
	v_mul_f32_e32 v212, v161, v161
	v_mul_f32_e32 v200, v162, v162
	v_mul_f32_e32 v198, v163, v163
	v_pk_add_f32 v[210:211], v[210:211], v[212:213]
	v_pk_add_f32 v[198:199], v[200:201], v[198:199]
	s_nop 0
	v_pk_add_f32 v[198:199], v[210:211], v[198:199]
	s_nop 0
	v_add_f32_e32 v1, v198, v199
	s_nop 1
	v_add_f32_dpp v1, v1, v1 quad_perm:[1,0,3,2] row_mask:0xf bank_mask:0xf
	s_nop 1
	v_add_f32_dpp v1, v1, v1 quad_perm:[2,3,0,1] row_mask:0xf bank_mask:0xf
	s_nop 1
	v_add_f32_dpp v1, v1, v1 row_half_mirror row_mask:0xf bank_mask:0xf
	s_nop 1
	v_add_f32_dpp v1, v1, v1 row_mirror row_mask:0xf bank_mask:0xf
	v_mov_b32_e32 v198, v1
	s_nop 1
	v_permlane16_swap_b32_e32 v1, v198
	v_add_f32_e32 v1, v1, v198
	v_mov_b32_e32 v198, v1
	s_nop 1
	v_permlane32_swap_b32_e32 v1, v198
	v_add_f32_e32 v1, v1, v198
	v_fmamk_f32 v1, v1, 0x3a000000, v196
	v_mul_f32_e32 v198, 0x4b800000, v1
	v_cmp_gt_f32_e32 vcc, s52, v1
	s_nop 1
	v_cndmask_b32_e32 v1, v1, v198, vcc
	v_rsq_f32_e32 v1, v1
	s_nop 0
	v_mul_f32_e32 v198, 0x45800000, v1
	v_cndmask_b32_e32 v198, v1, v198, vcc
	v_pk_mul_f32 v[134:135], v[134:135], v[198:199] op_sel_hi:[1,0]
	v_pk_mul_f32 v[132:133], v[132:133], v[198:199] op_sel_hi:[1,0]
	v_pk_fma_f32 v[200:201], v[70:71], v[134:135], v[74:75]
	v_pk_mul_f32 v[134:135], v[138:139], v[198:199] op_sel_hi:[1,0]
	v_pk_fma_f32 v[210:211], v[68:69], v[132:133], v[72:73]
	v_pk_mul_f32 v[132:133], v[136:137], v[198:199] op_sel_hi:[1,0]
	v_pk_fma_f32 v[136:137], v[78:79], v[134:135], v[82:83]
	v_max_f32_e64 v1, |v200|, |v201|
	v_pk_fma_f32 v[138:139], v[76:77], v[132:133], v[80:81]
	v_max_f32_e64 v132, |v136|, |v137|
	v_max3_f32 v1, |v210|, |v211|, v1
	v_max3_f32 v132, |v138|, |v139|, v132
	v_pk_mul_f32 v[134:135], v[142:143], v[198:199] op_sel_hi:[1,0]
	v_max3_f32 v1, v1, 0, v132
	v_pk_mul_f32 v[132:133], v[140:141], v[198:199] op_sel_hi:[1,0]
	v_pk_fma_f32 v[140:141], v[86:87], v[134:135], v[90:91]
	v_pk_fma_f32 v[142:143], v[84:85], v[132:133], v[88:89]
	v_max_f32_e64 v132, |v140|, |v141|
	v_max3_f32 v199, |v142|, |v143|, v132
	v_pk_mul_f32 v[134:135], v[146:147], v[198:199] op_sel_hi:[1,0]
	v_pk_mul_f32 v[132:133], v[144:145], v[198:199] op_sel_hi:[1,0]
	v_pk_fma_f32 v[144:145], v[94:95], v[134:135], v[98:99]
	v_pk_fma_f32 v[146:147], v[92:93], v[132:133], v[96:97]
	v_max_f32_e64 v132, |v144|, |v145|
	v_max3_f32 v132, |v146|, |v147|, v132
	v_pk_mul_f32 v[134:135], v[150:151], v[198:199] op_sel_hi:[1,0]
	v_max3_f32 v1, v1, v199, v132
	v_pk_mul_f32 v[132:133], v[148:149], v[198:199] op_sel_hi:[1,0]
	v_pk_fma_f32 v[148:149], v[102:103], v[134:135], v[106:107]
	v_pk_fma_f32 v[150:151], v[100:101], v[132:133], v[104:105]
	v_max_f32_e64 v132, |v148|, |v149|
	v_max3_f32 v199, |v150|, |v151|, v132
	v_pk_mul_f32 v[134:135], v[154:155], v[198:199] op_sel_hi:[1,0]
	v_pk_mul_f32 v[132:133], v[152:153], v[198:199] op_sel_hi:[1,0]
	v_pk_fma_f32 v[152:153], v[110:111], v[134:135], v[114:115]
	v_pk_fma_f32 v[154:155], v[108:109], v[132:133], v[112:113]
	v_max_f32_e64 v132, |v152|, |v153|
	v_max3_f32 v132, |v154|, |v155|, v132
	v_pk_mul_f32 v[134:135], v[158:159], v[198:199] op_sel_hi:[1,0]
	v_max3_f32 v1, v1, v199, v132
	v_pk_mul_f32 v[132:133], v[156:157], v[198:199] op_sel_hi:[1,0]
	v_pk_fma_f32 v[156:157], v[118:119], v[134:135], v[122:123]
	v_pk_fma_f32 v[158:159], v[116:117], v[132:133], v[120:121]
	v_max_f32_e64 v132, |v156|, |v157|
	v_max3_f32 v199, |v158|, |v159|, v132
	v_pk_mul_f32 v[132:133], v[162:163], v[198:199] op_sel_hi:[1,0]
	v_pk_mul_f32 v[134:135], v[160:161], v[198:199] op_sel_hi:[1,0]
	v_pk_fma_f32 v[132:133], v[126:127], v[132:133], v[130:131]
	v_pk_fma_f32 v[160:161], v[124:125], v[134:135], v[128:129]
; __device__ __forceinline__ unsigned pack_i8x4(float a, float b, float c, float d, float inv) { return q8u(a, inv) | (q8u(b, inv) << 8) | (q8u(c, inv) << 16) | (q8u(d, inv) << 24); }
; __device__ __forceinline__ float amax4(const f32x4& v) { return fmaxf(fmaxf(fabsf(v.x), fabsf(v.y)), fmaxf(fabsf(v.z), fabsf(v.w))); }
; __device__ __forceinline__ float wave_max(float v) {
; #pragma unroll
;     for (int o = 1; o < 64; o <<= 1) v = fmaxf(v, __shfl_xor(v, o));
;     return v;
; __device__ __forceinline__ void phase_norm1(const Params& p, const Ctx& F, const int l) {
;     ...
;             for (int j = 0; j < 8; ++j) { v[j] = v[j] * rstd * A[j] + Bv[j]; am = fmaxf(am, amax4(v[j])); }
;             am = fmaxf(wave_max(am), 1e-20f); const float inv = 127.f / am;
;             unsigned* xn = (unsigned*)((signed char*)F.r1 + ((size_t)b * TPB + t) * DM) + F.lane;
; #pragma unroll
;             for (int j = 0; j < 8; ++j) __builtin_nontemporal_store(pack_i8x4(v[j].x, v[j].y, v[j].z, v[j].w, inv), xn + 64 * j);
	v_max_f32_e64 v134, |v132|, |v133|
	v_max3_f32 v134, |v160|, |v161|, v134
	v_max3_f32 v1, v1, v199, v134
	s_nop 1
	v_max_f32_dpp v1, v1, v1 quad_perm:[1,0,3,2] row_mask:0xf bank_mask:0xf
	s_nop 1
	v_max_f32_dpp v1, v1, v1 quad_perm:[2,3,0,1] row_mask:0xf bank_mask:0xf
	s_nop 1
	v_max_f32_dpp v1, v1, v1 row_half_mirror row_mask:0xf bank_mask:0xf
	s_nop 1
	v_max_f32_dpp v1, v1, v1 row_mirror row_mask:0xf bank_mask:0xf
	v_mov_b32_e32 v134, v1
	s_nop 1
	v_permlane16_swap_b32_e32 v1, v134
	v_max_f32_e32 v1, v1, v134
	v_mov_b32_e32 v134, v1
	s_nop 1
	v_permlane32_swap_b32_e32 v1, v134
	v_max3_f32 v134, v1, v134, s53
	v_div_scale_f32 v1, s[0:1], v134, v134, s12
	v_rcp_f32_e32 v135, v1
	s_ashr_i32 s1, s20, 31
	s_add_u32 s0, s21, s20
	s_addc_u32 s1, 0, s1
	v_fma_f32 v162, -v1, v135, 1.0
	v_fmac_f32_e32 v135, v162, v135
	v_div_scale_f32 v162, vcc, s12, v134, s12
	v_mul_f32_e32 v163, v162, v135
	v_fma_f32 v198, -v1, v163, v162
	v_fmac_f32_e32 v163, v198, v135
	v_fma_f32 v1, -v1, v163, v162
	v_div_fmas_f32 v1, v1, v135, v163
	v_div_fixup_f32 v1, v1, v134, s12
	v_mul_f32_e32 v162, v211, v1
	v_mul_f32_e32 v199, v200, v1
	v_mul_f32_e32 v135, v210, v1
	v_rndne_f32_e32 v162, v162
	v_rndne_f32_e32 v199, v199
	v_mul_f32_e32 v200, v201, v1
	v_rndne_f32_e32 v135, v135
	v_cvt_i32_f32_e32 v198, v162
	v_cvt_i32_f32_e32 v199, v199
	v_rndne_f32_e32 v200, v200
	v_cvt_i32_f32_e32 v135, v135
	v_cvt_i32_f32_e32 v200, v200
	v_mul_f32_e32 v138, v138, v1
	v_mul_f32_e32 v137, v137, v1
	v_rndne_f32_e32 v138, v138
	v_mul_f32_e32 v139, v139, v1
	v_mul_f32_e32 v136, v136, v1
	v_rndne_f32_e32 v137, v137
	v_med3_i32 v198, v198, s80, v218
	v_med3_i32 v199, v199, s80, v218
	v_cvt_i32_f32_e32 v138, v138
	v_rndne_f32_e32 v139, v139
	v_rndne_f32_e32 v136, v136
	v_cvt_i32_f32_e32 v137, v137
	v_med3_i32 v135, v135, s80, v218
	v_lshlrev_b32_e32 v198, 8, v198
	v_lshlrev_b32_e32 v199, 16, v199
	v_med3_i32 v200, v200, s80, v218
	v_cvt_i32_f32_e32 v139, v139
	v_cvt_i32_f32_e32 v136, v136
	s_lshl_b64 s[0:1], s[0:1], 11
	v_and_b32_e32 v198, 0xff00, v198
	v_and_b32_e32 v199, 0xff0000, v199
	v_perm_b32 v135, v200, v135, s81
	v_lshl_add_u64 v[162:163], v[180:181], 0, s[0:1]
	v_or3_b32 v135, v135, v198, v199
	global_store_dword v[162:163], v135, off nt
	v_med3_i32 v135, v138, s80, v218
	v_med3_i32 v137, v137, s80, v218
	v_med3_i32 v138, v139, s80, v218
	v_med3_i32 v136, v136, s80, v218
	v_perm_b32 v135, v137, v135, s81
	v_mul_f32_e32 v137, v142, v1
	v_lshlrev_b32_e32 v138, 8, v138
	v_lshlrev_b32_e32 v136, 16, v136
	v_rndne_f32_e32 v137, v137
	v_and_b32_e32 v138, 0xff00, v138
	v_and_b32_e32 v136, 0xff0000, v136
	v_cvt_i32_f32_e32 v137, v137
	v_or3_b32 v135, v135, v138, v136
	v_mul_f32_e32 v138, v141, v1
	v_rndne_f32_e32 v138, v138
	v_cvt_i32_f32_e32 v138, v138
	v_mul_f32_e32 v139, v143, v1
	global_store_dword v[162:163], v135, off offset:256 nt
	v_med3_i32 v135, v137, s80, v218
	v_mul_f32_e32 v137, v140, v1
	v_rndne_f32_e32 v139, v139
	v_rndne_f32_e32 v137, v137
	v_cvt_i32_f32_e32 v139, v139
	v_cvt_i32_f32_e32 v137, v137
	v_med3_i32 v138, v138, s80, v218
	v_perm_b32 v135, v138, v135, s81
	v_mul_f32_e32 v138, v146, v1
	v_rndne_f32_e32 v138, v138
	v_med3_i32 v136, v139, s80, v218
	v_med3_i32 v137, v137, s80, v218
	v_cvt_i32_f32_e32 v138, v138
	v_lshlrev_b32_e32 v136, 8, v136
	v_lshlrev_b32_e32 v137, 16, v137
	v_and_b32_e32 v136, 0xff00, v136
	v_and_b32_e32 v137, 0xff0000, v137
	v_or3_b32 v135, v135, v136, v137
	global_store_dword v[162:163], v135, off offset:512 nt
	v_med3_i32 v135, v138, s80, v218
	v_mul_f32_e32 v138, v145, v1
	v_rndne_f32_e32 v138, v138
	v_cvt_i32_f32_e32 v138, v138
	v_mul_f32_e32 v139, v147, v1
	v_mul_f32_e32 v137, v144, v1
	v_rndne_f32_e32 v139, v139
	v_rndne_f32_e32 v137, v137
; __device__ __forceinline__ unsigned pack_i8x4(float a, float b, float c, float d, float inv) { return q8u(a, inv) | (q8u(b, inv) << 8) | (q8u(c, inv) << 16) | (q8u(d, inv) << 24); }
; __device__ __forceinline__ void phase_norm1(const Params& p, const Ctx& F, const int l) {
;     ...
;             am = fmaxf(wave_max(am), 1e-20f); const float inv = 127.f / am;
;             unsigned* xn = (unsigned*)((signed char*)F.r1 + ((size_t)b * TPB + t) * DM) + F.lane;
; #pragma unroll
;             for (int j = 0; j < 8; ++j) __builtin_nontemporal_store(pack_i8x4(v[j].x, v[j].y, v[j].z, v[j].w, inv), xn + 64 * j);
;             if (F.lane == 0) F.sax[b * TPB + t] = am * (1.f / 127.f);
	v_cvt_i32_f32_e32 v139, v139
	v_cvt_i32_f32_e32 v137, v137
	v_med3_i32 v138, v138, s80, v218
	v_perm_b32 v135, v138, v135, s81
	v_mul_f32_e32 v138, v150, v1
	v_rndne_f32_e32 v138, v138
	v_med3_i32 v136, v139, s80, v218
	v_med3_i32 v137, v137, s80, v218
	v_cvt_i32_f32_e32 v138, v138
	v_lshlrev_b32_e32 v136, 8, v136
	v_lshlrev_b32_e32 v137, 16, v137
	v_and_b32_e32 v136, 0xff00, v136
	v_and_b32_e32 v137, 0xff0000, v137
	v_or3_b32 v135, v135, v136, v137
	global_store_dword v[162:163], v135, off offset:768 nt
	v_med3_i32 v135, v138, s80, v218
	v_mul_f32_e32 v138, v149, v1
	v_rndne_f32_e32 v138, v138
	v_cvt_i32_f32_e32 v138, v138
	v_mul_f32_e32 v139, v151, v1
	v_mul_f32_e32 v137, v148, v1
	v_rndne_f32_e32 v139, v139
	v_rndne_f32_e32 v137, v137
	v_cvt_i32_f32_e32 v139, v139
	v_cvt_i32_f32_e32 v137, v137
	v_med3_i32 v138, v138, s80, v218
	v_perm_b32 v135, v138, v135, s81
	v_mul_f32_e32 v138, v154, v1
	v_rndne_f32_e32 v138, v138
	v_med3_i32 v136, v139, s80, v218
	v_med3_i32 v137, v137, s80, v218
	v_cvt_i32_f32_e32 v138, v138
	v_lshlrev_b32_e32 v136, 8, v136
	v_lshlrev_b32_e32 v137, 16, v137
	v_and_b32_e32 v136, 0xff00, v136
	v_and_b32_e32 v137, 0xff0000, v137
	v_or3_b32 v135, v135, v136, v137
	global_store_dword v[162:163], v135, off offset:1024 nt
	v_med3_i32 v135, v138, s80, v218
	v_mul_f32_e32 v138, v153, v1
	v_rndne_f32_e32 v138, v138
	v_cvt_i32_f32_e32 v138, v138
	v_mul_f32_e32 v139, v155, v1
	v_mul_f32_e32 v137, v152, v1
	v_rndne_f32_e32 v139, v139
	v_rndne_f32_e32 v137, v137
	v_cvt_i32_f32_e32 v139, v139
	v_cvt_i32_f32_e32 v137, v137
	v_med3_i32 v138, v138, s80, v218
	v_perm_b32 v135, v138, v135, s81
	v_mul_f32_e32 v138, v158, v1
	v_rndne_f32_e32 v138, v138
	v_med3_i32 v136, v139, s80, v218
	v_med3_i32 v137, v137, s80, v218
	v_cvt_i32_f32_e32 v138, v138
	v_lshlrev_b32_e32 v136, 8, v136
	v_lshlrev_b32_e32 v137, 16, v137
	v_and_b32_e32 v136, 0xff00, v136
	v_and_b32_e32 v137, 0xff0000, v137
	v_or3_b32 v135, v135, v136, v137
	v_mul_f32_e32 v139, v159, v1
	global_store_dword v[162:163], v135, off offset:1280 nt
	v_med3_i32 v135, v138, s80, v218
	v_mul_f32_e32 v138, v157, v1
	v_rndne_f32_e32 v139, v139
	v_rndne_f32_e32 v138, v138
	v_cvt_i32_f32_e32 v139, v139
	v_cvt_i32_f32_e32 v138, v138
	v_mul_f32_e32 v137, v156, v1
	v_rndne_f32_e32 v137, v137
	v_cvt_i32_f32_e32 v137, v137
	v_med3_i32 v136, v139, s80, v218
	v_med3_i32 v138, v138, s80, v218
	v_mul_f32_e32 v139, v161, v1
	v_mul_f32_e32 v132, v132, v1
	v_perm_b32 v135, v138, v135, s81
	v_mul_f32_e32 v138, v160, v1
	v_rndne_f32_e32 v139, v139
	v_rndne_f32_e32 v132, v132
	v_mul_f32_e32 v1, v133, v1
	v_rndne_f32_e32 v138, v138
	v_cvt_i32_f32_e32 v139, v139
	v_cvt_i32_f32_e32 v132, v132
	v_rndne_f32_e32 v1, v1
	v_med3_i32 v137, v137, s80, v218
	v_cvt_i32_f32_e32 v138, v138
	v_cvt_i32_f32_e32 v1, v1
	v_lshlrev_b32_e32 v136, 8, v136
	v_lshlrev_b32_e32 v137, 16, v137
	v_and_b32_e32 v136, 0xff00, v136
	v_and_b32_e32 v137, 0xff0000, v137
	v_or3_b32 v135, v135, v136, v137
	v_med3_i32 v136, v139, s80, v218
	v_med3_i32 v132, v132, s80, v218
	global_store_dword v[162:163], v135, off offset:1536 nt
	v_med3_i32 v135, v138, s80, v218
	v_lshlrev_b32_e32 v136, 8, v136
	v_lshlrev_b32_e32 v132, 16, v132
	v_med3_i32 v1, v1, s80, v218
	v_and_b32_e32 v136, 0xff00, v136
	v_and_b32_e32 v132, 0xff0000, v132
	v_perm_b32 v1, v1, v135, s81
	v_or3_b32 v1, v1, v136, v132
	global_store_dword v[162:163], v1, off offset:1792 nt
	s_and_saveexec_b64 s[0:1], s[6:7]
	s_cbranch_execz .LBB0_152
	s_add_i32 s12, s20, s21
	s_ashr_i32 s13, s12, 31
	s_lshl_b64 s[12:13], s[12:13], 2
	s_add_u32 s12, s26, s12
	s_addc_u32 s13, s27, s13
	v_mul_f32_e32 v1, 0x3c010204, v134
	global_store_dword v35, v1, s[12:13]
	s_branch .LBB0_152

; __device__ __forceinline__ void qkmma8(f32x16& p0, f32x16& p1, const i32x8 (&kf)[4], const i32x8 (&q8)[2], const f32x16& init) {
;   __builtin_amdgcn_s_setprio(1);
;   mfma8_32c(p0, kf[0], q8[0], init); mfma8_32c(p1, kf[1], q8[0], init); mfma8_32(p0, kf[2], q8[1]); mfma8_32(p1, kf[3], q8[1]);
;   __builtin_amdgcn_s_setprio(0);
; }
; __device__ __forceinline__ void qkt8(f32x16& p0, f32x16& p1, const LAS char* Ks, const i32x8 (&q8)[2], int r32, int hi, const f32x16& init) {
;   i32x8 kf[4]; kfrag8(kf, Ks, r32, hi); qkmma8(p0, p1, kf, q8, init);
; }
; __device__ __forceinline__ void finishSM8(f32x16& p0, f32x16& p1, float& l_reg, i32x8& pf) {
; #pragma unroll
;   for (int r = 0; r < 16; ++r) p1[r] = __builtin_amdgcn_exp2f(p1[r]);
;   float ps = 0;
; #pragma unroll
;   for (int r = 0; r < 16; ++r) ps += p0[r];
; #pragma unroll
;   for (int r = 0; r < 16; ++r) ps += p1[r];
;   { auto rr = __builtin_amdgcn_permlane32_swap(__float_as_uint(ps), __float_as_uint(ps), false, false);
;     ps = __uint_as_float(rr[0]) + __uint_as_float(rr[1]); }
;   l_reg += ps;
; #pragma unroll
;   for (int i = 0; i < 4; ++i) { pf[i] = cvt4_f8(p0[4 * i], p0[4 * i + 1], p0[4 * i + 2], p0[4 * i + 3]); pf[4 + i] = cvt4_f8(p1[4 * i], p1[4 * i + 1], p1[4 * i + 2], p1[4 * i + 3]); }
; }
; __device__ __forceinline__ void vfrag8(i32x8 (&vf)[4], const LAS char* Vs, int r32, int hi) {
;   const int xs = (r32 >> 1) & 3; const LAS char* vp = Vs + r32 * 64;
; #pragma unroll
; template <int MODE> __device__ __forceinline__ void attn_unit_c8(const AUnit& u, const bf16_t* __restrict__ P, const unsigned char* __restrict__ Kh, const unsigned char* __restrict__ Vh, const float* __restrict__ qn, bf16_t* __restrict__ O, LAS char* lds) {
;     ...
;   for (int j = 1; j + 1 < NT; j += 2) {
;     if (j + 3 < NT) DMA8(s2, j + 3);
;     { i32x8 vf[4]; SBAR(); { i32x8 kf[4]; kfrag8(kf, K_lds + (s0 * 2 + 1) * SHM8, r32, hi); qkmma8(pB0, pB1, kf, q8, acc0); }
;       vfrag8(vf, V_lds + (s0 * 2) * SHM8, r32, hi);
;       finishSM8(pA0, pA1, l_reg, pf); SBAR();
;       pvmma8(o, vf, pf); }
;     MASK8(pB0, pB1, j); EXP16(pB0);
;     { i32x8 vf[4]; SBAR(); { i32x8 kf[4]; kfrag8(kf, K_lds + (s1 * 2) * SHM8, r32, hi); qkmma8(pA0, pA1, kf, q8, acc0); }
;       vfrag8(vf, V_lds + (s0 * 2 + 1) * SHM8, r32, hi);
;       finishSM8(pB0, pB1, l_reg, pf); SBAR();
;       pvmma8(o, vf, pf); }
;     MASK8(pA0, pA1, j + 1); EXP16(pA0);
.LBB0_523:
	s_lshl_b32 s5, s0, 14
	v_add_u32_e32 v1, s5, v158
	v_add_u32_e32 v104, v1, v159
	v_add_u32_e32 v108, v1, v162
	ds_read_b128 v[100:103], v104 offset:57344
	ds_read_b128 v[182:185], v104 offset:61440
	ds_read_b128 v[104:107], v108 offset:57344
	ds_read_b128 v[186:189], v108 offset:61440
	v_add_u32_e32 v108, v1, v163
	v_add_u32_e32 v1, v1, v164
	ds_read_b128 v[202:205], v108 offset:57344
	ds_read_b128 v[230:233], v108 offset:61440
	ds_read_b128 v[206:209], v1 offset:57344
	ds_read_b128 v[234:237], v1 offset:61440
	s_setprio 1
	s_waitcnt lgkmcnt(0)
	v_mfma_f32_32x32x64_f8f6f4 v[116:131], v[100:107], v[132:139], v[68:83]
	v_mfma_f32_32x32x64_f8f6f4 v[100:115], v[182:189], v[132:139], v[68:83]
	s_nop 0
	v_mfma_f32_32x32x64_f8f6f4 v[116:131], v[202:209], v[140:147], v[116:131]
	v_mfma_f32_32x32x64_f8f6f4 v[100:115], v[230:237], v[140:147], v[100:115]
	s_setprio 0
	v_exp_f32_e32 v181, v84
	v_add_f32_e32 v84, 0, v179
	v_add_f32_e32 v84, v180, v84
	v_add_f32_e32 v84, v169, v84
	v_add_f32_e32 v84, v171, v84
	v_add_f32_e32 v84, v177, v84
	v_add_f32_e32 v84, v178, v84
	v_add_f32_e32 v84, v174, v84
	v_add_f32_e32 v84, v176, v84
	v_add_f32_e32 v84, v173, v84
	v_add_f32_e32 v84, v175, v84
	v_add_f32_e32 v84, v153, v84
	v_add_f32_e32 v84, v154, v84
	v_add_f32_e32 v84, v170, v84
	v_exp_f32_e32 v85, v85
	v_add_f32_e32 v84, v172, v84
	v_exp_f32_e32 v86, v86
	v_add_f32_e32 v84, v155, v84
	v_exp_f32_e32 v87, v87
	v_add_f32_e32 v84, v168, v84
	v_exp_f32_e32 v190, v88
	v_add_f32_e32 v84, v181, v84
	v_exp_f32_e32 v191, v89
	v_add_f32_e32 v84, v85, v84
	v_exp_f32_e32 v90, v90
	v_add_f32_e32 v84, v86, v84
	v_exp_f32_e32 v91, v91
	v_add_f32_e32 v84, v87, v84
	v_exp_f32_e32 v92, v92
	v_add_f32_e32 v84, v190, v84
	v_exp_f32_e32 v93, v93
	v_add_f32_e32 v84, v191, v84
	v_exp_f32_e32 v94, v94
	v_add_f32_e32 v84, v90, v84
	v_exp_f32_e32 v95, v95
	v_add_f32_e32 v84, v91, v84
	v_exp_f32_e32 v96, v96
	v_add_f32_e32 v84, v92, v84
	v_exp_f32_e32 v97, v97
	v_add_f32_e32 v84, v93, v84
	v_exp_f32_e32 v98, v98
	v_add_f32_e32 v84, v94, v84
	v_add_u32_e32 v1, s5, v165
	v_exp_f32_e32 v99, v99
	v_add_f32_e32 v84, v95, v84
	v_cvt_pk_fp8_f32 v88, v181, v85
	v_cvt_pk_fp8_f32 v89, v190, v191
	v_add_u32_e32 v192, v1, v166
	v_add_f32_e32 v84, v96, v84
	v_add_u32_e32 v1, v1, v167
	ds_read_b128 v[182:185], v192
	ds_read_b128 v[202:205], v192 offset:2048
	ds_read_b128 v[186:189], v1
	ds_read_b128 v[206:209], v1 offset:2048
	ds_read_b128 v[230:233], v192 offset:4096
	ds_read_b128 v[238:241], v192 offset:6144
	ds_read_b128 v[234:237], v1 offset:4096
	ds_read_b128 v[242:245], v1 offset:6144
	v_add_f32_e32 v84, v97, v84
	v_add_f32_e32 v84, v98, v84
	v_add_f32_e32 v152, v99, v84
	v_cvt_pk_fp8_f32 v88, v86, v87 op_sel:[0,0,1]
	v_cvt_pk_fp8_f32 v89, v90, v91 op_sel:[0,0,1]
	v_cvt_pk_fp8_f32 v84, v179, v180
	v_cvt_pk_fp8_f32 v85, v177, v178
	v_cvt_pk_fp8_f32 v86, v173, v175
	v_cvt_pk_fp8_f32 v90, v92, v93
	v_cvt_pk_fp8_f32 v87, v170, v172
	v_cvt_pk_fp8_f32 v91, v96, v97
	v_cvt_pk_fp8_f32 v84, v169, v171 op_sel:[0,0,1]
	v_cvt_pk_fp8_f32 v85, v174, v176 op_sel:[0,0,1]
	v_cvt_pk_fp8_f32 v86, v153, v154 op_sel:[0,0,1]
	v_cvt_pk_fp8_f32 v90, v94, v95 op_sel:[0,0,1]
	v_cvt_pk_fp8_f32 v87, v155, v168 op_sel:[0,0,1]
	v_cvt_pk_fp8_f32 v91, v98, v99 op_sel:[0,0,1]
	v_mov_b32_e32 v154, v152
	s_nop 1
	v_permlane32_swap_b32_e32 v152, v154
	s_setprio 1
	s_waitcnt lgkmcnt(0)
	v_mfma_f32_32x32x64_f8f6f4 v[52:67], v[84:91], v[182:189], v[52:67]
	v_mfma_f32_32x32x64_f8f6f4 v[36:51], v[84:91], v[202:209], v[36:51]
	v_mfma_f32_32x32x64_f8f6f4 v[18:33], v[84:91], v[230:237], v[18:33]
	v_mfma_f32_32x32x64_f8f6f4 v[2:17], v[84:91], v[238:245], v[2:17]
	s_setprio 0
	v_exp_f32_e32 v193, v116
	v_exp_f32_e32 v194, v117
	v_exp_f32_e32 v195, v118
	v_exp_f32_e32 v198, v119
	v_exp_f32_e32 v199, v120
	v_exp_f32_e32 v200, v121
	v_exp_f32_e32 v201, v122
	v_exp_f32_e32 v210, v123
	v_exp_f32_e32 v211, v124
	v_exp_f32_e32 v212, v125
	v_exp_f32_e32 v213, v126
	v_exp_f32_e32 v214, v127
	v_exp_f32_e32 v215, v128
	v_exp_f32_e32 v216, v129
	v_exp_f32_e32 v229, v130
	v_exp_f32_e32 v230, v131
	v_lshl_add_u32 v92, s4, 14, v158
	v_add_u32_e32 v88, v92, v159
	v_add_u32_e32 v93, v92, v162
	ds_read_b128 v[84:87], v88 offset:49152
	ds_read_b128 v[168:171], v88 offset:53248
	ds_read_b128 v[88:91], v93 offset:49152
	ds_read_b128 v[172:175], v93 offset:53248
	v_add_u32_e32 v93, v92, v163
	v_add_u32_e32 v92, v92, v164
	ds_read_b128 v[176:179], v93 offset:49152
	ds_read_b128 v[184:187], v93 offset:53248
	ds_read_b128 v[180:183], v92 offset:49152
	ds_read_b128 v[188:191], v92 offset:53248
	s_setprio 1
	s_waitcnt lgkmcnt(0)
; #define SBAR() __builtin_amdgcn_sched_barrier(0)
; #define DWAIT() asm volatile("s_waitcnt vmcnt(0)" ::: "memory")
; __device__ __forceinline__ int cvt4_f8(float a, float b, float c, float d) { int w = 0; w = __builtin_amdgcn_cvt_pk_fp8_f32(a, b, w, false); w = __builtin_amdgcn_cvt_pk_fp8_f32(c, d, w, true); return w; }
; #define MASK8(p0_, p1_, j_) do { if constexpr (MODE == 1) mask_tile<1>(p0_, p1_, u, (j_), wid, r32, hi, (const LAS float*)nullptr); } while (0)
; #define DWAIT() asm volatile("s_waitcnt vmcnt(0)" ::: "memory")
; #define EXP16(p_) do { _Pragma("unroll") for (int r = 0; r < 16; ++r) p_[r] = __builtin_amdgcn_exp2f(p_[r]); } while (0)
; #define DWAIT() asm volatile("s_waitcnt vmcnt(0)" ::: "memory")
; __device__ __forceinline__ void finishSM8(f32x16& p0, f32x16& p1, float& l_reg, i32x8& pf) {
; #pragma unroll
;   for (int r = 0; r < 16; ++r) p1[r] = __builtin_amdgcn_exp2f(p1[r]);
;   float ps = 0;
; #pragma unroll
;   for (int r = 0; r < 16; ++r) ps += p0[r];
; #pragma unroll
;   for (int r = 0; r < 16; ++r) ps += p1[r];
;   { auto rr = __builtin_amdgcn_permlane32_swap(__float_as_uint(ps), __float_as_uint(ps), false, false);
;     ps = __uint_as_float(rr[0]) + __uint_as_float(rr[1]); }
;   l_reg += ps;
; #pragma unroll
;   for (int i = 0; i < 4; ++i) { pf[i] = cvt4_f8(p0[4 * i], p0[4 * i + 1], p0[4 * i + 2], p0[4 * i + 3]); pf[4 + i] = cvt4_f8(p1[4 * i], p1[4 * i + 1], p1[4 * i + 2], p1[4 * i + 3]); }
; template <int MODE> __device__ __forceinline__ void attn_unit_c8(const AUnit& u, const bf16_t* __restrict__ P, const unsigned char* __restrict__ Kh, const unsigned char* __restrict__ Vh, const float* __restrict__ qn, bf16_t* __restrict__ O, LAS char* lds) {
;     ...
;     { i32x8 vf[4]; SBAR(); { i32x8 kf[4]; kfrag8(kf, K_lds + (s1 * 2) * SHM8, r32, hi); qkmma8(pA0, pA1, kf, q8, acc0); }
;       vfrag8(vf, V_lds + (s0 * 2 + 1) * SHM8, r32, hi);
;       finishSM8(pB0, pB1, l_reg, pf); SBAR();
;       pvmma8(o, vf, pf); }
;     MASK8(pA0, pA1, j + 1); EXP16(pA0);
;     DWAIT(); __syncthreads();
;     { const int t_ = s0; s0 = s1; s1 = s2; s2 = t_; }
	v_mfma_f32_32x32x64_f8f6f4 v[116:131], v[84:91], v[132:139], v[68:83]
	v_mfma_f32_32x32x64_f8f6f4 v[84:99], v[168:175], v[132:139], v[68:83]
	s_nop 0
	v_mfma_f32_32x32x64_f8f6f4 v[116:131], v[176:183], v[140:147], v[116:131]
	v_mfma_f32_32x32x64_f8f6f4 v[84:99], v[184:191], v[140:147], v[84:99]
	s_setprio 0
	ds_read_b128 v[168:171], v192 offset:8192
	ds_read_b128 v[176:179], v192 offset:10240
	ds_read_b128 v[172:175], v1 offset:8192
	ds_read_b128 v[180:183], v1 offset:10240
	ds_read_b128 v[184:187], v192 offset:12288
	ds_read_b128 v[202:205], v192 offset:14336
	ds_read_b128 v[188:191], v1 offset:12288
	ds_read_b128 v[206:209], v1 offset:14336
	v_exp_f32_e32 v1, v100
	v_add_f32_e32 v100, 0, v193
	v_add_f32_e32 v100, v194, v100
	v_add_f32_e32 v100, v195, v100
	v_add_f32_e32 v100, v198, v100
	v_add_f32_e32 v100, v199, v100
	v_add_f32_e32 v100, v200, v100
	v_add_f32_e32 v100, v201, v100
	v_add_f32_e32 v100, v210, v100
	v_add_f32_e32 v100, v211, v100
	v_add_f32_e32 v100, v212, v100
	v_add_f32_e32 v100, v213, v100
	v_add_f32_e32 v100, v214, v100
	v_add_f32_e32 v100, v215, v100
	v_exp_f32_e32 v101, v101
	v_add_f32_e32 v100, v216, v100
	v_exp_f32_e32 v102, v102
	v_add_f32_e32 v100, v229, v100
	v_exp_f32_e32 v103, v103
	v_add_f32_e32 v100, v230, v100
	v_exp_f32_e32 v192, v104
	v_add_f32_e32 v100, v1, v100
	v_exp_f32_e32 v231, v105
	v_add_f32_e32 v100, v101, v100
	v_exp_f32_e32 v106, v106
	v_add_f32_e32 v100, v102, v100
	v_exp_f32_e32 v107, v107
	v_add_f32_e32 v100, v103, v100
	v_exp_f32_e32 v108, v108
	v_add_f32_e32 v100, v192, v100
	v_exp_f32_e32 v109, v109
	v_add_f32_e32 v100, v231, v100
	v_exp_f32_e32 v110, v110
	v_add_f32_e32 v100, v106, v100
	v_exp_f32_e32 v111, v111
	v_add_f32_e32 v100, v107, v100
	v_exp_f32_e32 v112, v112
	v_add_f32_e32 v100, v108, v100
	v_exp_f32_e32 v113, v113
	v_add_f32_e32 v100, v109, v100
	v_exp_f32_e32 v114, v114
	v_add_f32_e32 v100, v110, v100
	v_exp_f32_e32 v115, v115
	v_add_f32_e32 v100, v111, v100
	v_cvt_pk_fp8_f32 v104, v1, v101
	v_cvt_pk_fp8_f32 v105, v192, v231
	v_add_f32_e32 v100, v112, v100
	v_add_f32_e32 v100, v113, v100
	v_add_f32_e32 v100, v114, v100
	v_add_f32_e32 v153, v115, v100
	v_cvt_pk_fp8_f32 v104, v102, v103 op_sel:[0,0,1]
	v_cvt_pk_fp8_f32 v105, v106, v107 op_sel:[0,0,1]
	v_cvt_pk_fp8_f32 v100, v193, v194
	v_cvt_pk_fp8_f32 v101, v199, v200
	v_cvt_pk_fp8_f32 v102, v211, v212
	v_cvt_pk_fp8_f32 v106, v108, v109
	v_cvt_pk_fp8_f32 v103, v215, v216
	v_cvt_pk_fp8_f32 v107, v112, v113
	v_mov_b32_e32 v155, v153
	s_nop 1
	v_permlane32_swap_b32_e32 v153, v155
	v_cvt_pk_fp8_f32 v100, v195, v198 op_sel:[0,0,1]
	v_cvt_pk_fp8_f32 v101, v201, v210 op_sel:[0,0,1]
	v_cvt_pk_fp8_f32 v102, v213, v214 op_sel:[0,0,1]
	v_cvt_pk_fp8_f32 v106, v110, v111 op_sel:[0,0,1]
	v_cvt_pk_fp8_f32 v103, v229, v230 op_sel:[0,0,1]
	v_cvt_pk_fp8_f32 v107, v114, v115 op_sel:[0,0,1]
	v_pk_add_f32 v[108:109], v[152:153], v[154:155]
	s_setprio 1
	s_waitcnt lgkmcnt(0)
	v_mfma_f32_32x32x64_f8f6f4 v[52:67], v[100:107], v[168:175], v[52:67]
	v_mfma_f32_32x32x64_f8f6f4 v[36:51], v[100:107], v[176:183], v[36:51]
	v_mfma_f32_32x32x64_f8f6f4 v[18:33], v[100:107], v[184:191], v[18:33]
	v_mfma_f32_32x32x64_f8f6f4 v[2:17], v[100:107], v[202:209], v[2:17]
	s_setprio 0
	v_exp_f32_e32 v179, v116
	v_exp_f32_e32 v180, v117
	v_exp_f32_e32 v169, v118
	v_exp_f32_e32 v171, v119
	v_exp_f32_e32 v177, v120
	v_exp_f32_e32 v178, v121
	v_exp_f32_e32 v174, v122
	v_exp_f32_e32 v176, v123
	v_exp_f32_e32 v173, v124
	v_exp_f32_e32 v175, v125
	v_exp_f32_e32 v153, v126
	v_exp_f32_e32 v154, v127
	v_exp_f32_e32 v170, v128
	v_exp_f32_e32 v172, v129
	v_exp_f32_e32 v155, v130
	v_exp_f32_e32 v168, v131
	s_waitcnt vmcnt(0)
	v_add_f32_e32 v1, v34, v108
	s_mov_b64 s[6:7], 0x4000
	v_add_f32_e32 v34, v1, v109
	s_add_i32 s23, s23, 2
	v_lshl_add_u64 v[148:149], v[148:149], 0, s[6:7]
	v_lshl_add_u64 v[150:151], v[150:151], 0, s[6:7]
	s_and_b64 vcc, exec, s[2:3]
	s_waitcnt vmcnt(0)
	s_barrier
	s_cbranch_vccnz .LBB0_525
	s_mov_b32 s24, s0
	s_mov_b32 s0, s4
	s_branch .LBB0_521

; __device__ __forceinline__ void qkmma8(f32x16& p0, f32x16& p1, const i32x8 (&kf)[4], const i32x8 (&q8)[2], const f32x16& init) {
;   __builtin_amdgcn_s_setprio(1);
;   mfma8_32c(p0, kf[0], q8[0], init); mfma8_32c(p1, kf[1], q8[0], init); mfma8_32(p0, kf[2], q8[1]); mfma8_32(p1, kf[3], q8[1]);
;   __builtin_amdgcn_s_setprio(0);
; }
; __device__ __forceinline__ void qkt8(f32x16& p0, f32x16& p1, const LAS char* Ks, const i32x8 (&q8)[2], int r32, int hi, const f32x16& init) {
;   i32x8 kf[4]; kfrag8(kf, Ks, r32, hi); qkmma8(p0, p1, kf, q8, init);
; }
; __device__ __forceinline__ void finishSM8(f32x16& p0, f32x16& p1, float& l_reg, i32x8& pf) {
; #pragma unroll
;   for (int r = 0; r < 16; ++r) p1[r] = __builtin_amdgcn_exp2f(p1[r]);
;   float ps = 0;
; #pragma unroll
;   for (int r = 0; r < 16; ++r) ps += p0[r];
; #pragma unroll
;   for (int r = 0; r < 16; ++r) ps += p1[r];
;   { auto rr = __builtin_amdgcn_permlane32_swap(__float_as_uint(ps), __float_as_uint(ps), false, false);
;     ps = __uint_as_float(rr[0]) + __uint_as_float(rr[1]); }
;   l_reg += ps;
; #pragma unroll
;   for (int i = 0; i < 4; ++i) { pf[i] = cvt4_f8(p0[4 * i], p0[4 * i + 1], p0[4 * i + 2], p0[4 * i + 3]); pf[4 + i] = cvt4_f8(p1[4 * i], p1[4 * i + 1], p1[4 * i + 2], p1[4 * i + 3]); }
; }
; __device__ __forceinline__ void vfrag8(i32x8 (&vf)[4], const LAS char* Vs, int r32, int hi) {
;   const int xs = (r32 >> 1) & 3; const LAS char* vp = Vs + r32 * 64;
; #pragma unroll
; template <int MODE> __device__ __forceinline__ void attn_unit_c8(const AUnit& u, const bf16_t* __restrict__ P, const unsigned char* __restrict__ Kh, const unsigned char* __restrict__ Vh, const float* __restrict__ qn, bf16_t* __restrict__ O, LAS char* lds) {
;     ...
;   for (int j = 1; j + 1 < NT; j += 2) {
;     if (j + 3 < NT) DMA8(s2, j + 3);
;     { i32x8 vf[4]; SBAR(); { i32x8 kf[4]; kfrag8(kf, K_lds + (s0 * 2 + 1) * SHM8, r32, hi); qkmma8(pB0, pB1, kf, q8, acc0); }
;       vfrag8(vf, V_lds + (s0 * 2) * SHM8, r32, hi);
;       finishSM8(pA0, pA1, l_reg, pf); SBAR();
;       pvmma8(o, vf, pf); }
;     MASK8(pB0, pB1, j); EXP16(pB0);
;     { i32x8 vf[4]; SBAR(); { i32x8 kf[4]; kfrag8(kf, K_lds + (s1 * 2) * SHM8, r32, hi); qkmma8(pA0, pA1, kf, q8, acc0); }
;       vfrag8(vf, V_lds + (s0 * 2 + 1) * SHM8, r32, hi);
;       finishSM8(pB0, pB1, l_reg, pf); SBAR();
;       pvmma8(o, vf, pf); }
;     MASK8(pA0, pA1, j + 1); EXP16(pA0);
.LBB0_543:
	s_lshl_b32 s7, s0, 14
	v_add_u32_e32 v1, s7, v161
	v_add_u32_e32 v104, v1, v163
	v_add_u32_e32 v108, v1, v164
	ds_read_b128 v[100:103], v104 offset:57344
	ds_read_b128 v[186:189], v104 offset:61440
	ds_read_b128 v[104:107], v108 offset:57344
	ds_read_b128 v[190:193], v108 offset:61440
	v_add_u32_e32 v108, v1, v167
	v_add_u32_e32 v1, v1, v168
	ds_read_b128 v[202:205], v108 offset:57344
	ds_read_b128 v[224:227], v108 offset:61440
	ds_read_b128 v[206:209], v1 offset:57344
	ds_read_b128 v[228:231], v1 offset:61440
	s_setprio 1
	s_waitcnt lgkmcnt(0)
	v_mfma_f32_32x32x64_f8f6f4 v[116:131], v[100:107], v[132:139], v[68:83]
	v_mfma_f32_32x32x64_f8f6f4 v[100:115], v[186:193], v[132:139], v[68:83]
	s_nop 0
	v_mfma_f32_32x32x64_f8f6f4 v[116:131], v[202:209], v[140:147], v[116:131]
	v_mfma_f32_32x32x64_f8f6f4 v[100:115], v[224:231], v[140:147], v[100:115]
	s_setprio 0
	v_exp_f32_e32 v185, v84
	v_add_f32_e32 v84, 0, v183
	v_add_f32_e32 v84, v184, v84
	v_add_f32_e32 v84, v173, v84
	v_add_f32_e32 v84, v175, v84
	v_add_f32_e32 v84, v181, v84
	v_add_f32_e32 v84, v182, v84
	v_add_f32_e32 v84, v178, v84
	v_add_f32_e32 v84, v180, v84
	v_add_f32_e32 v84, v177, v84
	v_add_f32_e32 v84, v179, v84
	v_add_f32_e32 v84, v155, v84
	v_add_f32_e32 v84, v156, v84
	v_add_f32_e32 v84, v174, v84
	v_exp_f32_e32 v85, v85
	v_add_f32_e32 v84, v176, v84
	v_exp_f32_e32 v86, v86
	v_add_f32_e32 v84, v157, v84
	v_exp_f32_e32 v87, v87
	v_add_f32_e32 v84, v172, v84
	v_exp_f32_e32 v194, v88
	v_add_f32_e32 v84, v185, v84
	v_exp_f32_e32 v195, v89
	v_add_f32_e32 v84, v85, v84
	v_exp_f32_e32 v90, v90
	v_add_f32_e32 v84, v86, v84
	v_exp_f32_e32 v91, v91
	v_add_f32_e32 v84, v87, v84
	v_exp_f32_e32 v92, v92
	v_add_f32_e32 v84, v194, v84
	v_exp_f32_e32 v93, v93
	v_add_f32_e32 v84, v195, v84
	v_exp_f32_e32 v94, v94
	v_add_f32_e32 v84, v90, v84
	v_exp_f32_e32 v95, v95
	v_add_f32_e32 v84, v91, v84
	v_exp_f32_e32 v96, v96
	v_add_f32_e32 v84, v92, v84
	v_exp_f32_e32 v97, v97
	v_add_f32_e32 v84, v93, v84
	v_exp_f32_e32 v98, v98
	v_add_f32_e32 v84, v94, v84
	v_add_u32_e32 v1, s7, v169
	v_exp_f32_e32 v99, v99
	v_add_f32_e32 v84, v95, v84
	v_cvt_pk_fp8_f32 v88, v185, v85
	v_cvt_pk_fp8_f32 v89, v194, v195
	v_add_u32_e32 v198, v1, v170
	v_add_f32_e32 v84, v96, v84
	v_add_u32_e32 v1, v1, v171
	ds_read_b128 v[186:189], v198
	ds_read_b128 v[202:205], v198 offset:2048
	ds_read_b128 v[190:193], v1
	ds_read_b128 v[206:209], v1 offset:2048
	ds_read_b128 v[224:227], v198 offset:4096
	ds_read_b128 v[232:235], v198 offset:6144
	ds_read_b128 v[228:231], v1 offset:4096
	ds_read_b128 v[236:239], v1 offset:6144
	v_add_f32_e32 v84, v97, v84
	v_add_f32_e32 v84, v98, v84
	v_add_f32_e32 v154, v99, v84
	v_cvt_pk_fp8_f32 v88, v86, v87 op_sel:[0,0,1]
	v_cvt_pk_fp8_f32 v89, v90, v91 op_sel:[0,0,1]
	v_cvt_pk_fp8_f32 v84, v183, v184
	v_cvt_pk_fp8_f32 v85, v181, v182
	v_cvt_pk_fp8_f32 v86, v177, v179
	v_cvt_pk_fp8_f32 v90, v92, v93
	v_cvt_pk_fp8_f32 v87, v174, v176
	v_cvt_pk_fp8_f32 v91, v96, v97
	v_cvt_pk_fp8_f32 v84, v173, v175 op_sel:[0,0,1]
	v_cvt_pk_fp8_f32 v85, v178, v180 op_sel:[0,0,1]
	v_cvt_pk_fp8_f32 v86, v155, v156 op_sel:[0,0,1]
	v_cvt_pk_fp8_f32 v90, v94, v95 op_sel:[0,0,1]
	v_cvt_pk_fp8_f32 v87, v157, v172 op_sel:[0,0,1]
	v_cvt_pk_fp8_f32 v91, v98, v99 op_sel:[0,0,1]
	v_mov_b32_e32 v156, v154
	s_nop 1
	v_permlane32_swap_b32_e32 v154, v156
	s_setprio 1
	s_waitcnt lgkmcnt(0)
	v_mfma_f32_32x32x64_f8f6f4 v[2:17], v[84:91], v[186:193], v[2:17]
	v_mfma_f32_32x32x64_f8f6f4 v[18:33], v[84:91], v[202:209], v[18:33]
	v_mfma_f32_32x32x64_f8f6f4 v[36:51], v[84:91], v[224:231], v[36:51]
	v_mfma_f32_32x32x64_f8f6f4 v[52:67], v[84:91], v[232:239], v[52:67]
	s_setprio 0
	v_exp_f32_e32 v199, v116
	v_exp_f32_e32 v200, v117
	v_exp_f32_e32 v201, v118
	v_exp_f32_e32 v210, v119
	v_exp_f32_e32 v211, v120
	v_exp_f32_e32 v212, v121
	v_exp_f32_e32 v213, v122
	v_exp_f32_e32 v214, v123
	v_exp_f32_e32 v215, v124
	v_exp_f32_e32 v216, v125
	v_exp_f32_e32 v224, v126
	v_exp_f32_e32 v225, v127
	v_exp_f32_e32 v226, v128
	v_exp_f32_e32 v227, v129
	v_exp_f32_e32 v228, v130
	v_exp_f32_e32 v229, v131
	v_lshl_add_u32 v92, s6, 14, v161
	v_add_u32_e32 v88, v92, v163
	v_add_u32_e32 v93, v92, v164
	ds_read_b128 v[84:87], v88 offset:49152
	ds_read_b128 v[172:175], v88 offset:53248
	ds_read_b128 v[88:91], v93 offset:49152
	ds_read_b128 v[176:179], v93 offset:53248
	v_add_u32_e32 v93, v92, v167
	v_add_u32_e32 v92, v92, v168
	ds_read_b128 v[180:183], v93 offset:49152
	ds_read_b128 v[188:191], v93 offset:53248
	ds_read_b128 v[184:187], v92 offset:49152
	ds_read_b128 v[192:195], v92 offset:53248
	s_setprio 1
	s_waitcnt lgkmcnt(0)
; #define SBAR() __builtin_amdgcn_sched_barrier(0)
; #define DWAIT() asm volatile("s_waitcnt vmcnt(0)" ::: "memory")
; __device__ __forceinline__ int cvt4_f8(float a, float b, float c, float d) { int w = 0; w = __builtin_amdgcn_cvt_pk_fp8_f32(a, b, w, false); w = __builtin_amdgcn_cvt_pk_fp8_f32(c, d, w, true); return w; }
; #define MASK8(p0_, p1_, j_) do { if constexpr (MODE == 1) mask_tile<1>(p0_, p1_, u, (j_), wid, r32, hi, (const LAS float*)nullptr); } while (0)
; #define DWAIT() asm volatile("s_waitcnt vmcnt(0)" ::: "memory")
; #define EXP16(p_) do { _Pragma("unroll") for (int r = 0; r < 16; ++r) p_[r] = __builtin_amdgcn_exp2f(p_[r]); } while (0)
; #define DWAIT() asm volatile("s_waitcnt vmcnt(0)" ::: "memory")
; __device__ __forceinline__ void finishSM8(f32x16& p0, f32x16& p1, float& l_reg, i32x8& pf) {
; #pragma unroll
;   for (int r = 0; r < 16; ++r) p1[r] = __builtin_amdgcn_exp2f(p1[r]);
;   float ps = 0;
; #pragma unroll
;   for (int r = 0; r < 16; ++r) ps += p0[r];
; #pragma unroll
;   for (int r = 0; r < 16; ++r) ps += p1[r];
;   { auto rr = __builtin_amdgcn_permlane32_swap(__float_as_uint(ps), __float_as_uint(ps), false, false);
;     ps = __uint_as_float(rr[0]) + __uint_as_float(rr[1]); }
;   l_reg += ps;
; #pragma unroll
;   for (int i = 0; i < 4; ++i) { pf[i] = cvt4_f8(p0[4 * i], p0[4 * i + 1], p0[4 * i + 2], p0[4 * i + 3]); pf[4 + i] = cvt4_f8(p1[4 * i], p1[4 * i + 1], p1[4 * i + 2], p1[4 * i + 3]); }
; template <int MODE> __device__ __forceinline__ void attn_unit_c8(const AUnit& u, const bf16_t* __restrict__ P, const unsigned char* __restrict__ Kh, const unsigned char* __restrict__ Vh, const float* __restrict__ qn, bf16_t* __restrict__ O, LAS char* lds) {
;     ...
;     { i32x8 vf[4]; SBAR(); { i32x8 kf[4]; kfrag8(kf, K_lds + (s1 * 2) * SHM8, r32, hi); qkmma8(pA0, pA1, kf, q8, acc0); }
;       vfrag8(vf, V_lds + (s0 * 2 + 1) * SHM8, r32, hi);
;       finishSM8(pB0, pB1, l_reg, pf); SBAR();
;       pvmma8(o, vf, pf); }
;     MASK8(pA0, pA1, j + 1); EXP16(pA0);
;     DWAIT(); __syncthreads();
;     { const int t_ = s0; s0 = s1; s1 = s2; s2 = t_; }
	v_mfma_f32_32x32x64_f8f6f4 v[116:131], v[84:91], v[132:139], v[68:83]
	v_mfma_f32_32x32x64_f8f6f4 v[84:99], v[172:179], v[132:139], v[68:83]
	s_nop 0
	v_mfma_f32_32x32x64_f8f6f4 v[116:131], v[180:187], v[140:147], v[116:131]
	v_mfma_f32_32x32x64_f8f6f4 v[84:99], v[188:195], v[140:147], v[84:99]
	s_setprio 0
	ds_read_b128 v[172:175], v198 offset:8192
	ds_read_b128 v[180:183], v198 offset:10240
	ds_read_b128 v[176:179], v1 offset:8192
	ds_read_b128 v[184:187], v1 offset:10240
	ds_read_b128 v[188:191], v198 offset:12288
	ds_read_b128 v[202:205], v198 offset:14336
	ds_read_b128 v[192:195], v1 offset:12288
	ds_read_b128 v[206:209], v1 offset:14336
	v_exp_f32_e32 v1, v100
	v_add_f32_e32 v100, 0, v199
	v_add_f32_e32 v100, v200, v100
	v_add_f32_e32 v100, v201, v100
	v_add_f32_e32 v100, v210, v100
	v_add_f32_e32 v100, v211, v100
	v_add_f32_e32 v100, v212, v100
	v_add_f32_e32 v100, v213, v100
	v_add_f32_e32 v100, v214, v100
	v_add_f32_e32 v100, v215, v100
	v_add_f32_e32 v100, v216, v100
	v_add_f32_e32 v100, v224, v100
	v_add_f32_e32 v100, v225, v100
	v_add_f32_e32 v100, v226, v100
	v_exp_f32_e32 v101, v101
	v_add_f32_e32 v100, v227, v100
	v_exp_f32_e32 v102, v102
	v_add_f32_e32 v100, v228, v100
	v_exp_f32_e32 v103, v103
	v_add_f32_e32 v100, v229, v100
	v_exp_f32_e32 v198, v104
	v_add_f32_e32 v100, v1, v100
	v_exp_f32_e32 v230, v105
	v_add_f32_e32 v100, v101, v100
	v_exp_f32_e32 v106, v106
	v_add_f32_e32 v100, v102, v100
	v_exp_f32_e32 v107, v107
	v_add_f32_e32 v100, v103, v100
	v_exp_f32_e32 v108, v108
	v_add_f32_e32 v100, v198, v100
	v_exp_f32_e32 v109, v109
	v_add_f32_e32 v100, v230, v100
	v_exp_f32_e32 v110, v110
	v_add_f32_e32 v100, v106, v100
	v_exp_f32_e32 v111, v111
	v_add_f32_e32 v100, v107, v100
	v_exp_f32_e32 v112, v112
	v_add_f32_e32 v100, v108, v100
	v_exp_f32_e32 v113, v113
	v_add_f32_e32 v100, v109, v100
	v_exp_f32_e32 v114, v114
	v_add_f32_e32 v100, v110, v100
	v_exp_f32_e32 v115, v115
	v_add_f32_e32 v100, v111, v100
	v_cvt_pk_fp8_f32 v104, v1, v101
	v_cvt_pk_fp8_f32 v105, v198, v230
	v_add_f32_e32 v100, v112, v100
	v_add_f32_e32 v100, v113, v100
	v_add_f32_e32 v100, v114, v100
	v_add_f32_e32 v155, v115, v100
	v_cvt_pk_fp8_f32 v104, v102, v103 op_sel:[0,0,1]
	v_cvt_pk_fp8_f32 v105, v106, v107 op_sel:[0,0,1]
	v_cvt_pk_fp8_f32 v100, v199, v200
	v_cvt_pk_fp8_f32 v101, v211, v212
	v_cvt_pk_fp8_f32 v102, v215, v216
	v_cvt_pk_fp8_f32 v106, v108, v109
	v_cvt_pk_fp8_f32 v103, v226, v227
	v_cvt_pk_fp8_f32 v107, v112, v113
	v_mov_b32_e32 v157, v155
	s_nop 1
	v_permlane32_swap_b32_e32 v155, v157
	v_cvt_pk_fp8_f32 v100, v201, v210 op_sel:[0,0,1]
	v_cvt_pk_fp8_f32 v101, v213, v214 op_sel:[0,0,1]
	v_cvt_pk_fp8_f32 v102, v224, v225 op_sel:[0,0,1]
	v_cvt_pk_fp8_f32 v106, v110, v111 op_sel:[0,0,1]
	v_cvt_pk_fp8_f32 v103, v228, v229 op_sel:[0,0,1]
	v_cvt_pk_fp8_f32 v107, v114, v115 op_sel:[0,0,1]
	v_pk_add_f32 v[108:109], v[154:155], v[156:157]
	s_setprio 1
	s_waitcnt lgkmcnt(0)
	v_mfma_f32_32x32x64_f8f6f4 v[2:17], v[100:107], v[172:179], v[2:17]
	v_mfma_f32_32x32x64_f8f6f4 v[18:33], v[100:107], v[180:187], v[18:33]
	v_mfma_f32_32x32x64_f8f6f4 v[36:51], v[100:107], v[188:195], v[36:51]
	v_mfma_f32_32x32x64_f8f6f4 v[52:67], v[100:107], v[202:209], v[52:67]
	s_setprio 0
	v_exp_f32_e32 v183, v116
	v_exp_f32_e32 v184, v117
	v_exp_f32_e32 v173, v118
	v_exp_f32_e32 v175, v119
	v_exp_f32_e32 v181, v120
	v_exp_f32_e32 v182, v121
	v_exp_f32_e32 v178, v122
	v_exp_f32_e32 v180, v123
	v_exp_f32_e32 v177, v124
	v_exp_f32_e32 v179, v125
	v_exp_f32_e32 v155, v126
	v_exp_f32_e32 v156, v127
	v_exp_f32_e32 v174, v128
	v_exp_f32_e32 v176, v129
	v_exp_f32_e32 v157, v130
	v_exp_f32_e32 v172, v131
	s_waitcnt vmcnt(0)
	s_add_i32 s62, s62, 2
	v_add_f32_e32 v1, v34, v108
	s_add_u32 s2, s2, 0x4000
	v_add_f32_e32 v34, v1, v109
	s_addc_u32 s3, s3, 0
	s_and_b64 vcc, exec, s[4:5]
	s_waitcnt vmcnt(0)
	s_barrier
	s_cbranch_vccnz .LBB0_545
	s_mov_b32 s4, s0
	s_mov_b32 s0, s6
	s_branch .LBB0_541

; #define LAS __attribute__((address_space(3)))
; __device__ __forceinline__ void qkmma8(f32x16& p0, f32x16& p1, const i32x8 (&kf)[4], const i32x8 (&q8)[2], const f32x16& init) {
;   __builtin_amdgcn_s_setprio(1);
;   mfma8_32c(p0, kf[0], q8[0], init); mfma8_32c(p1, kf[1], q8[0], init); mfma8_32(p0, kf[2], q8[1]); mfma8_32(p1, kf[3], q8[1]);
;   __builtin_amdgcn_s_setprio(0);
; }
; __device__ __forceinline__ void qkt8(f32x16& p0, f32x16& p1, const LAS char* Ks, const i32x8 (&q8)[2], int r32, int hi, const f32x16& init) {
;   i32x8 kf[4]; kfrag8(kf, Ks, r32, hi); qkmma8(p0, p1, kf, q8, init);
; }
; __device__ __forceinline__ void finishSM8(f32x16& p0, f32x16& p1, float& l_reg, i32x8& pf) {
; #pragma unroll
;   for (int r = 0; r < 16; ++r) p1[r] = __builtin_amdgcn_exp2f(p1[r]);
;   float ps = 0;
; #pragma unroll
;   for (int r = 0; r < 16; ++r) ps += p0[r];
; #pragma unroll
;   for (int r = 0; r < 16; ++r) ps += p1[r];
;   { auto rr = __builtin_amdgcn_permlane32_swap(__float_as_uint(ps), __float_as_uint(ps), false, false);
;     ps = __uint_as_float(rr[0]) + __uint_as_float(rr[1]); }
;   l_reg += ps;
; #pragma unroll
;   for (int i = 0; i < 4; ++i) { pf[i] = cvt4_f8(p0[4 * i], p0[4 * i + 1], p0[4 * i + 2], p0[4 * i + 3]); pf[4 + i] = cvt4_f8(p1[4 * i], p1[4 * i + 1], p1[4 * i + 2], p1[4 * i + 3]); }
; }
; __device__ __forceinline__ void vfrag8(i32x8 (&vf)[4], const LAS char* Vs, int r32, int hi) {
;   const int xs = (r32 >> 1) & 3; const LAS char* vp = Vs + r32 * 64;
; #pragma unroll
;   for (int d0 = 0; d0 < 4; ++d0) vf[d0] = cat8(*reinterpret_cast<const LAS i32x4*>(vp + d0 * 2048 + (((2 * hi) ^ xs) << 4)), *reinterpret_cast<const LAS i32x4*>(vp + d0 * 2048 + (((2 * hi + 1) ^ xs) << 4)));
; }
; template <int MODE> __device__ __forceinline__ void attn_unit_c8(const AUnit& u, const bf16_t* __restrict__ P, const unsigned char* __restrict__ Kh, const unsigned char* __restrict__ Vh, const float* __restrict__ qn, bf16_t* __restrict__ O, LAS char* lds) {
;     ...
;   for (int j = 1; j + 1 < NT; j += 2) {
;     if (j + 3 < NT) DMA8(s2, j + 3);
;     { i32x8 vf[4]; SBAR(); { i32x8 kf[4]; kfrag8(kf, K_lds + (s0 * 2 + 1) * SHM8, r32, hi); qkmma8(pB0, pB1, kf, q8, acc0); }
;       vfrag8(vf, V_lds + (s0 * 2) * SHM8, r32, hi);
;       finishSM8(pA0, pA1, l_reg, pf); SBAR();
;       pvmma8(o, vf, pf); }
;     MASK8(pB0, pB1, j); EXP16(pB0);
.LBB0_603:
	s_lshl_b32 s0, s5, 14
	v_add_u32_e32 v1, s0, v168
	v_add_u32_e32 v34, v1, v160
	v_add_u32_e32 v108, v1, v161
	ds_read_b128 v[100:103], v34 offset:57344
	ds_read_b128 v[202:205], v34 offset:61440
	ds_read_b128 v[104:107], v108 offset:57344
	ds_read_b128 v[206:209], v108 offset:61440
	v_add_u32_e32 v34, v1, v162
	v_add_u32_e32 v1, v1, v163
	ds_read_b128 v[224:227], v34 offset:57344
	ds_read_b128 v[232:235], v34 offset:61440
	ds_read_b128 v[228:231], v1 offset:57344
	ds_read_b128 v[236:239], v1 offset:61440
	s_setprio 1
	s_waitcnt lgkmcnt(0)
	v_mfma_f32_32x32x64_f8f6f4 v[116:131], v[100:107], v[132:139], v[68:83]
	v_mfma_f32_32x32x64_f8f6f4 v[100:115], v[202:209], v[132:139], v[68:83]
	s_nop 0
	v_mfma_f32_32x32x64_f8f6f4 v[116:131], v[224:231], v[140:147], v[116:131]
	v_mfma_f32_32x32x64_f8f6f4 v[100:115], v[232:239], v[140:147], v[100:115]
	s_setprio 0
	v_add_u32_e32 v1, s0, v185
	v_add_u32_e32 v34, v1, v164
	v_add_u32_e32 v186, v1, v165
	v_exp_f32_e32 v1, v84
	v_add_f32_e32 v84, 0, v183
	v_add_f32_e32 v84, v184, v84
	v_add_f32_e32 v84, v174, v84
	v_add_f32_e32 v84, v176, v84
	v_add_f32_e32 v84, v181, v84
	v_add_f32_e32 v84, v182, v84
	v_add_f32_e32 v84, v179, v84
	v_add_f32_e32 v84, v180, v84
	v_add_f32_e32 v84, v177, v84
	v_add_f32_e32 v84, v178, v84
	v_add_f32_e32 v84, v169, v84
	v_add_f32_e32 v84, v170, v84
	v_add_f32_e32 v84, v173, v84
	v_exp_f32_e32 v85, v85
	v_add_f32_e32 v84, v175, v84
	v_exp_f32_e32 v187, v86
	v_add_f32_e32 v84, v171, v84
	v_exp_f32_e32 v188, v87
	v_add_f32_e32 v84, v172, v84
	v_exp_f32_e32 v88, v88
	v_add_f32_e32 v84, v1, v84
	v_exp_f32_e32 v89, v89
	v_add_f32_e32 v84, v85, v84
	v_exp_f32_e32 v189, v90
	v_add_f32_e32 v84, v187, v84
	v_exp_f32_e32 v191, v91
	v_add_f32_e32 v84, v188, v84
	v_exp_f32_e32 v192, v92
	v_add_f32_e32 v84, v88, v84
	v_exp_f32_e32 v93, v93
	v_add_f32_e32 v84, v89, v84
	v_exp_f32_e32 v94, v94
	v_add_f32_e32 v84, v189, v84
	ds_read_b128 v[202:205], v34
	ds_read_b128 v[224:227], v34 offset:2048
	ds_read_b128 v[206:209], v186
	ds_read_b128 v[228:231], v186 offset:2048
	ds_read_b128 v[232:235], v34 offset:4096
	ds_read_b128 v[240:243], v34 offset:6144
	ds_read_b128 v[236:239], v186 offset:4096
	ds_read_b128 v[244:247], v186 offset:6144
	v_exp_f32_e32 v95, v95
	v_add_f32_e32 v84, v191, v84
	v_exp_f32_e32 v96, v96
	v_add_f32_e32 v84, v192, v84
	v_exp_f32_e32 v97, v97
	v_add_f32_e32 v84, v93, v84
	v_exp_f32_e32 v98, v98
	v_add_f32_e32 v84, v94, v84
	v_exp_f32_e32 v99, v99
	v_add_f32_e32 v84, v95, v84
	v_add_f32_e32 v84, v96, v84
	v_add_f32_e32 v84, v97, v84
	v_cvt_pk_fp8_f32 v91, v88, v89
	v_cvt_pk_fp8_f32 v92, v192, v93
	v_add_f32_e32 v84, v98, v84
	v_cvt_pk_fp8_f32 v86, v183, v184
	v_cvt_pk_fp8_f32 v90, v1, v85
	v_cvt_pk_fp8_f32 v87, v181, v182
	v_cvt_pk_fp8_f32 v88, v177, v178
	v_cvt_pk_fp8_f32 v89, v173, v175
	v_cvt_pk_fp8_f32 v93, v96, v97
	v_add_f32_e32 v84, v99, v84
	v_mov_b32_e32 v85, v84
	s_nop 1
	v_permlane32_swap_b32_e32 v84, v85
	v_cvt_pk_fp8_f32 v86, v174, v176 op_sel:[0,0,1]
	v_cvt_pk_fp8_f32 v90, v187, v188 op_sel:[0,0,1]
	v_cvt_pk_fp8_f32 v87, v179, v180 op_sel:[0,0,1]
	v_cvt_pk_fp8_f32 v91, v189, v191 op_sel:[0,0,1]
	v_cvt_pk_fp8_f32 v88, v169, v170 op_sel:[0,0,1]
	v_cvt_pk_fp8_f32 v92, v94, v95 op_sel:[0,0,1]
	v_cvt_pk_fp8_f32 v89, v171, v172 op_sel:[0,0,1]
	v_cvt_pk_fp8_f32 v93, v98, v99 op_sel:[0,0,1]
	s_setprio 1
	s_waitcnt lgkmcnt(0)
	v_mfma_f32_32x32x64_f8f6f4 v[52:67], v[86:93], v[202:209], v[52:67]
	v_mfma_f32_32x32x64_f8f6f4 v[36:51], v[86:93], v[224:231], v[36:51]
	v_mfma_f32_32x32x64_f8f6f4 v[18:33], v[86:93], v[232:239], v[18:33]
	v_mfma_f32_32x32x64_f8f6f4 v[2:17], v[86:93], v[240:247], v[2:17]
	s_setprio 0
	s_cmp_lt_u32 s1, 4
	s_cbranch_scc1 .LBB0_605
; #define LAS __attribute__((address_space(3)))
; template <int MODE> __device__ __forceinline__ void mask_tile(f32x16& p0, f32x16& p1, const AUnit& u, int j, int wid, int r32, int hi, const LAS float* btab) {
;   if (MODE == 0 || j < 4) return;
;   if (MODE == 1) {
;     const int qpos = u.pa + wid * 32 + r32, k0 = u.pb + (j - 4) * 64 + 4 * hi;
; #pragma unroll
;     for (int r = 0; r < 16; ++r) { const int d = qpos - (k0 + (r & 3) + 8 * (r >> 2));
;       p0[r] = (d <= 128 && d >= -128) ? p0[r] : -1e30f; const int d1 = d - 32; p1[r] = (d1 <= 128 && d1 >= -128) ? p1[r] : -1e30f; }
	v_add_u32_e32 v1, 0x7b, v190
	s_movk_i32 s18, 0x101
	v_cmp_gt_u32_e32 vcc, s18, v1
	v_add_u32_e32 v1, 0x5b, v190
	s_nop 0
	v_cndmask_b32_e32 v116, v221, v116, vcc
	v_cmp_gt_u32_e32 vcc, s18, v1
	v_add_u32_e32 v1, 0x7a, v190
	s_nop 0
	v_cndmask_b32_e32 v100, v221, v100, vcc
	v_cmp_gt_u32_e32 vcc, s18, v1
	v_add_u32_e32 v1, 0x5a, v190
	s_nop 0
	v_cndmask_b32_e32 v117, v221, v117, vcc
	v_cmp_gt_u32_e32 vcc, s18, v1
	v_add_u32_e32 v1, 0x79, v190
	s_nop 0
	v_cndmask_b32_e32 v101, v221, v101, vcc
	v_cmp_gt_u32_e32 vcc, s18, v1
	v_add_u32_e32 v1, 0x59, v190
	s_nop 0
	v_cndmask_b32_e32 v118, v221, v118, vcc
	v_cmp_gt_u32_e32 vcc, s18, v1
	v_add_u32_e32 v1, 0x78, v190
	s_nop 0
	v_cndmask_b32_e32 v102, v221, v102, vcc
	v_cmp_gt_u32_e32 vcc, s18, v1
	v_add_u32_e32 v1, 0x58, v190
	s_nop 0
	v_cndmask_b32_e32 v119, v221, v119, vcc
	v_cmp_gt_u32_e32 vcc, s18, v1
	v_add_u32_e32 v1, 0x73, v190
	s_nop 0
	v_cndmask_b32_e32 v103, v221, v103, vcc
	v_cmp_gt_u32_e32 vcc, s18, v1
	v_add_u32_e32 v1, 0x53, v190
	s_nop 0
	v_cndmask_b32_e32 v120, v221, v120, vcc
	v_cmp_gt_u32_e32 vcc, s18, v1
	v_add_u32_e32 v1, 0x72, v190
	s_nop 0
	v_cndmask_b32_e32 v104, v221, v104, vcc
	v_cmp_gt_u32_e32 vcc, s18, v1
	v_add_u32_e32 v1, 0x52, v190
	s_nop 0
	v_cndmask_b32_e32 v121, v221, v121, vcc
	v_cmp_gt_u32_e32 vcc, s18, v1
	v_add_u32_e32 v1, 0x71, v190
	s_nop 0
	v_cndmask_b32_e32 v105, v221, v105, vcc
	v_cmp_gt_u32_e32 vcc, s18, v1
	v_add_u32_e32 v1, 0x51, v190
	s_nop 0
	v_cndmask_b32_e32 v122, v221, v122, vcc
	v_cmp_gt_u32_e32 vcc, s18, v1
	v_add_u32_e32 v1, 0x70, v190
	s_nop 0
	v_cndmask_b32_e32 v106, v221, v106, vcc
	v_cmp_gt_u32_e32 vcc, s18, v1
	v_add_u32_e32 v1, 0x50, v190
	s_nop 0
	v_cndmask_b32_e32 v123, v221, v123, vcc
	v_cmp_gt_u32_e32 vcc, s18, v1
	v_add_u32_e32 v1, 0x6b, v190
	s_nop 0
	v_cndmask_b32_e32 v107, v221, v107, vcc
	v_cmp_gt_u32_e32 vcc, s18, v1
	v_add_u32_e32 v1, 0x4b, v190
	s_nop 0
	v_cndmask_b32_e32 v124, v221, v124, vcc
	v_cmp_gt_u32_e32 vcc, s18, v1
	v_add_u32_e32 v1, 0x6a, v190
	s_nop 0
	v_cndmask_b32_e32 v108, v221, v108, vcc
	v_cmp_gt_u32_e32 vcc, s18, v1
	v_add_u32_e32 v1, 0x4a, v190
	s_nop 0
	v_cndmask_b32_e32 v125, v221, v125, vcc
	v_cmp_gt_u32_e32 vcc, s18, v1
	v_add_u32_e32 v1, 0x69, v190
	s_nop 0
	v_cndmask_b32_e32 v109, v221, v109, vcc
	v_cmp_gt_u32_e32 vcc, s18, v1
	v_add_u32_e32 v1, 0x49, v190
	s_nop 0
	v_cndmask_b32_e32 v126, v221, v126, vcc
	v_cmp_gt_u32_e32 vcc, s18, v1
	v_add_u32_e32 v1, 0x68, v190
	s_nop 0
	v_cndmask_b32_e32 v110, v221, v110, vcc
	v_cmp_gt_u32_e32 vcc, s18, v1
	v_add_u32_e32 v1, 0x48, v190
	s_nop 0
	v_cndmask_b32_e32 v127, v221, v127, vcc
	v_cmp_gt_u32_e32 vcc, s18, v1
	v_add_u32_e32 v1, 0x63, v190
	s_nop 0
	v_cndmask_b32_e32 v111, v221, v111, vcc
	v_cmp_gt_u32_e32 vcc, s18, v1
	v_add_u32_e32 v1, 0x43, v190
	s_nop 0
	v_cndmask_b32_e32 v128, v221, v128, vcc
	v_cmp_gt_u32_e32 vcc, s18, v1
	v_add_u32_e32 v1, 0x62, v190
	s_nop 0
	v_cndmask_b32_e32 v112, v221, v112, vcc
	v_cmp_gt_u32_e32 vcc, s18, v1
	v_add_u32_e32 v1, 0x42, v190
	s_nop 0
	v_cndmask_b32_e32 v129, v221, v129, vcc
	v_cmp_gt_u32_e32 vcc, s18, v1
	v_add_u32_e32 v1, 0x61, v190
	s_nop 0
	v_cndmask_b32_e32 v113, v221, v113, vcc
	v_cmp_gt_u32_e32 vcc, s18, v1
	v_add_u32_e32 v1, 0x41, v190
	s_nop 0
	v_cndmask_b32_e32 v130, v221, v130, vcc
	v_cmp_gt_u32_e32 vcc, s18, v1
	v_add_u32_e32 v1, 0x60, v190
	s_nop 0
	v_cndmask_b32_e32 v114, v221, v114, vcc
	v_cmp_gt_u32_e32 vcc, s18, v1
	v_add_u32_e32 v1, 64, v190
	s_nop 0
	v_cndmask_b32_e32 v131, v221, v131, vcc
	v_cmp_gt_u32_e32 vcc, s18, v1
	s_nop 1
	v_cndmask_b32_e32 v115, v221, v115, vcc
	s_branch .LBB0_606

; __device__ __forceinline__ float bflo(unsigned w) { return __uint_as_float(w << 16); }
; __device__ __forceinline__ float bfhi(unsigned w) { return __uint_as_float(w & 0xffff0000u); }
; __device__ __forceinline__ void phase_norm2(const Params& p, const Ctx& F, const int l) {
;     ...
;         { const float* xlat = l == 0 ? p.x : p.out; const float* xctx = l == 0 ? p.ctx : F.xc;
;           const float* xs0 = isctx ? xctx + ((size_t)b * CTXL + t) * DM : xlat + ((size_t)b * SEQ + (t - CTXL)) * DM;
;           const float* xs1 = two ? xlat + ((size_t)b * SEQ + (tB - CTXL)) * DM : xs0;
;           const bf16_t* d0p = F.dlt + ((size_t)b * TPB + t) * DM + 4 * F.lane; const bf16_t* d1p = F.dlt + ((size_t)b * TPB + (two ? tB : t)) * DM + 4 * F.lane;
; #pragma unroll
;           for (int j = 0; j < 8; ++j) { f32x4 x0 = __builtin_nontemporal_load((const f32x4*)xs0 + F.lane + 64 * j), x1 = __builtin_nontemporal_load((const f32x4*)xs1 + F.lane + 64 * j);
;               const u32x2 e0 = __builtin_nontemporal_load((const u32x2*)(d0p + 256 * j)), e1 = __builtin_nontemporal_load((const u32x2*)(d1p + 256 * j));
;               x0 += (f32x4){bflo(e0.x), bfhi(e0.x), bflo(e0.y), bfhi(e0.y)}; x1 += (f32x4){bflo(e1.x), bfhi(e1.x), bflo(e1.y), bfhi(e1.y)};
; #pragma unroll
;               for (int c = 0; c < 4; ++c) vv[j][c] = (f32x2){x0[c], x1[c]}; } }
.LBB0_918:
	s_waitcnt vmcnt(19)
	v_lshlrev_b32_e32 v185, 16, v182
	v_lshlrev_b32_e32 v184, 16, v180
	v_mov_b32_e32 v186, v124
	v_mov_b32_e32 v187, v128
	v_pk_add_f32 v[184:185], v[186:187], v[184:185]
	v_and_b32_e32 v187, 0xffff0000, v182
	v_and_b32_e32 v186, 0xffff0000, v180
	v_mov_b32_e32 v128, v125
	v_pk_add_f32 v[128:129], v[128:129], v[186:187]
	v_lshlrev_b32_e32 v125, 16, v183
	v_lshlrev_b32_e32 v124, 16, v181
	v_mov_b32_e32 v186, v126
	v_mov_b32_e32 v187, v130
	v_pk_add_f32 v[186:187], v[186:187], v[124:125]
	v_and_b32_e32 v125, 0xffff0000, v183
	v_and_b32_e32 v124, 0xffff0000, v181
	v_mov_b32_e32 v130, v127
	v_pk_add_f32 v[130:131], v[130:131], v[124:125]
	s_waitcnt vmcnt(18)
	v_lshlrev_b32_e32 v125, 16, v178
	v_lshlrev_b32_e32 v124, 16, v176
	v_mov_b32_e32 v126, v116
	v_mov_b32_e32 v127, v120
	v_pk_add_f32 v[180:181], v[126:127], v[124:125]
	v_and_b32_e32 v125, 0xffff0000, v178
	v_and_b32_e32 v124, 0xffff0000, v176
	v_mov_b32_e32 v120, v117
	v_pk_add_f32 v[116:117], v[120:121], v[124:125]
	v_lshlrev_b32_e32 v121, 16, v179
	v_lshlrev_b32_e32 v120, 16, v177
	v_mov_b32_e32 v124, v118
	v_mov_b32_e32 v125, v122
	v_pk_add_f32 v[120:121], v[124:125], v[120:121]
	v_and_b32_e32 v125, 0xffff0000, v179
	v_and_b32_e32 v124, 0xffff0000, v177
	v_mov_b32_e32 v122, v119
	v_pk_add_f32 v[122:123], v[122:123], v[124:125]
	s_waitcnt vmcnt(17)
	v_lshlrev_b32_e32 v119, 16, v174
	v_lshlrev_b32_e32 v118, 16, v172
	v_mov_b32_e32 v124, v108
	v_mov_b32_e32 v125, v112
	v_pk_add_f32 v[176:177], v[124:125], v[118:119]
	v_and_b32_e32 v119, 0xffff0000, v174
	v_and_b32_e32 v118, 0xffff0000, v172
	v_mov_b32_e32 v112, v109
	v_pk_add_f32 v[178:179], v[112:113], v[118:119]
	v_lshlrev_b32_e32 v109, 16, v175
	v_lshlrev_b32_e32 v108, 16, v173
	v_mov_b32_e32 v112, v110
	v_mov_b32_e32 v113, v114
	v_pk_add_f32 v[182:183], v[112:113], v[108:109]
	v_and_b32_e32 v109, 0xffff0000, v175
	v_and_b32_e32 v108, 0xffff0000, v173
	v_mov_b32_e32 v114, v111
	v_pk_add_f32 v[172:173], v[114:115], v[108:109]
	s_waitcnt vmcnt(16)
	v_lshlrev_b32_e32 v109, 16, v168
	v_lshlrev_b32_e32 v108, 16, v164
	v_mov_b32_e32 v110, v100
	v_mov_b32_e32 v111, v104
	v_pk_add_f32 v[174:175], v[110:111], v[108:109]
	v_and_b32_e32 v109, 0xffff0000, v168
	v_and_b32_e32 v108, 0xffff0000, v164
	v_mov_b32_e32 v104, v101
	v_pk_add_f32 v[100:101], v[104:105], v[108:109]
	v_lshlrev_b32_e32 v105, 16, v169
	v_lshlrev_b32_e32 v104, 16, v165
	v_mov_b32_e32 v108, v102
	v_mov_b32_e32 v109, v106
	v_pk_add_f32 v[104:105], v[108:109], v[104:105]
	v_and_b32_e32 v109, 0xffff0000, v169
	v_and_b32_e32 v108, 0xffff0000, v165
	v_mov_b32_e32 v106, v103
	v_pk_add_f32 v[106:107], v[106:107], v[108:109]
	s_waitcnt vmcnt(3)
	v_lshlrev_b32_e32 v103, 16, v170
	v_lshlrev_b32_e32 v102, 16, v166
	v_mov_b32_e32 v108, v92
	v_mov_b32_e32 v109, v96
	v_pk_add_f32 v[164:165], v[108:109], v[102:103]
	v_and_b32_e32 v103, 0xffff0000, v170
	v_and_b32_e32 v102, 0xffff0000, v166
	v_mov_b32_e32 v96, v93
	v_pk_add_f32 v[168:169], v[96:97], v[102:103]
	v_lshlrev_b32_e32 v93, 16, v171
	v_lshlrev_b32_e32 v92, 16, v167
	v_mov_b32_e32 v96, v94
	v_mov_b32_e32 v97, v98
	v_pk_add_f32 v[188:189], v[96:97], v[92:93]
	v_and_b32_e32 v93, 0xffff0000, v171
	v_and_b32_e32 v92, 0xffff0000, v167
	v_mov_b32_e32 v98, v95
	v_pk_add_f32 v[166:167], v[98:99], v[92:93]
	s_waitcnt vmcnt(2)
	v_lshlrev_b32_e32 v93, 16, v162
	v_lshlrev_b32_e32 v92, 16, v160
	v_mov_b32_e32 v94, v84
	v_mov_b32_e32 v95, v88
	v_pk_add_f32 v[170:171], v[94:95], v[92:93]
	v_and_b32_e32 v93, 0xffff0000, v162
	v_and_b32_e32 v92, 0xffff0000, v160
	v_mov_b32_e32 v88, v85
	v_pk_add_f32 v[84:85], v[88:89], v[92:93]
	v_lshlrev_b32_e32 v89, 16, v163
	v_lshlrev_b32_e32 v88, 16, v161
	v_mov_b32_e32 v92, v86
	v_mov_b32_e32 v93, v90
	v_pk_add_f32 v[88:89], v[92:93], v[88:89]
	v_and_b32_e32 v93, 0xffff0000, v163
	v_and_b32_e32 v92, 0xffff0000, v161
	v_mov_b32_e32 v90, v87
	v_pk_add_f32 v[90:91], v[90:91], v[92:93]
	s_waitcnt vmcnt(1)
	v_lshlrev_b32_e32 v87, 16, v158
	v_lshlrev_b32_e32 v86, 16, v156
	v_mov_b32_e32 v92, v76
	v_mov_b32_e32 v93, v80
	v_pk_add_f32 v[160:161], v[92:93], v[86:87]
	v_and_b32_e32 v87, 0xffff0000, v158
	v_and_b32_e32 v86, 0xffff0000, v156
	v_mov_b32_e32 v80, v77
	v_pk_add_f32 v[162:163], v[80:81], v[86:87]
	v_lshlrev_b32_e32 v77, 16, v159
	v_lshlrev_b32_e32 v76, 16, v157
	v_mov_b32_e32 v80, v78
	v_mov_b32_e32 v81, v82
	v_pk_add_f32 v[198:199], v[80:81], v[76:77]
	v_and_b32_e32 v77, 0xffff0000, v159
	v_and_b32_e32 v76, 0xffff0000, v157
	v_mov_b32_e32 v82, v79
	v_pk_add_f32 v[156:157], v[82:83], v[76:77]
	s_waitcnt vmcnt(0)
; __device__ __forceinline__ float wave_sum(float v) {
; #pragma unroll
;     for (int o = 1; o < 64; o <<= 1) v += __shfl_xor(v, o);
;     return v;
; __device__ __forceinline__ void phase_norm2(const Params& p, const Ctx& F, const int l) {
;     ...
;         f32x2 ss = {0.f, 0.f};
; #pragma unroll
;         for (int j = 0; j < 8; ++j)
; #pragma unroll
;             for (int c = 0; c < 4; ++c) ss += vv[j][c] * vv[j][c];
;         const f32x2 rstd = {rsqrtf(wave_sum(ss.x) * (1.f / DM) + EPS), rsqrtf(wave_sum(ss.y) * (1.f / DM) + EPS)};
;         f32x2 am = {0.f, 0.f};
; #pragma unroll
;         for (int j = 0; j < 8; ++j)
; #pragma unroll
;             for (int c = 0; c < 4; ++c) { vv[j][c] = vv[j][c] * rstd * A[j][c] + Bv[j][c]; am = __builtin_elementwise_max(am, __builtin_elementwise_abs(vv[j][c])); }
	v_lshlrev_b32_e32 v77, 16, v154
	v_lshlrev_b32_e32 v76, 16, v152
	v_mov_b32_e32 v78, v68
	v_mov_b32_e32 v79, v72
	v_pk_add_f32 v[158:159], v[78:79], v[76:77]
	v_and_b32_e32 v77, 0xffff0000, v154
	v_and_b32_e32 v76, 0xffff0000, v152
	v_mov_b32_e32 v72, v69
	v_pk_add_f32 v[72:73], v[72:73], v[76:77]
	v_lshlrev_b32_e32 v69, 16, v155
	v_lshlrev_b32_e32 v68, 16, v153
	v_mov_b32_e32 v76, v70
	v_mov_b32_e32 v77, v74
	v_pk_add_f32 v[200:201], v[76:77], v[68:69]
	v_and_b32_e32 v69, 0xffff0000, v155
	v_and_b32_e32 v68, 0xffff0000, v153
	v_mov_b32_e32 v74, v71
	v_pk_add_f32 v[74:75], v[74:75], v[68:69]
	v_pk_mul_f32 v[68:69], v[128:129], v[128:129]
	s_mov_b32 s0, 0x3a000000
	v_pk_fma_f32 v[68:69], v[184:185], v[184:185], v[68:69]
	s_mov_b32 s30, 0x45800000
	v_pk_fma_f32 v[68:69], v[186:187], v[186:187], v[68:69]
	v_mov_b32_e32 v34, v9
	v_pk_fma_f32 v[68:69], v[130:131], v[130:131], v[68:69]
	s_mov_b32 s52, 0x800000
	v_pk_fma_f32 v[68:69], v[180:181], v[180:181], v[68:69]
	s_nop 0
	v_pk_fma_f32 v[68:69], v[116:117], v[116:117], v[68:69]
	s_nop 0
	v_pk_fma_f32 v[68:69], v[120:121], v[120:121], v[68:69]
	s_nop 0
	v_pk_fma_f32 v[68:69], v[122:123], v[122:123], v[68:69]
	s_nop 0
	v_pk_fma_f32 v[68:69], v[176:177], v[176:177], v[68:69]
	s_nop 0
	v_pk_fma_f32 v[68:69], v[178:179], v[178:179], v[68:69]
	s_nop 0
	v_pk_fma_f32 v[68:69], v[182:183], v[182:183], v[68:69]
	s_nop 0
	v_pk_fma_f32 v[68:69], v[172:173], v[172:173], v[68:69]
	s_nop 0
	v_pk_fma_f32 v[68:69], v[174:175], v[174:175], v[68:69]
	s_nop 0
	v_pk_fma_f32 v[68:69], v[100:101], v[100:101], v[68:69]
	s_nop 0
	v_pk_fma_f32 v[68:69], v[104:105], v[104:105], v[68:69]
	s_nop 0
	v_pk_fma_f32 v[68:69], v[106:107], v[106:107], v[68:69]
	s_nop 0
	v_pk_fma_f32 v[68:69], v[164:165], v[164:165], v[68:69]
	s_nop 0
	v_pk_fma_f32 v[68:69], v[168:169], v[168:169], v[68:69]
	s_nop 0
	v_pk_fma_f32 v[68:69], v[188:189], v[188:189], v[68:69]
	s_nop 0
	v_pk_fma_f32 v[68:69], v[166:167], v[166:167], v[68:69]
	s_nop 0
	v_pk_fma_f32 v[68:69], v[170:171], v[170:171], v[68:69]
	s_nop 0
	v_pk_fma_f32 v[68:69], v[84:85], v[84:85], v[68:69]
	s_nop 0
	v_pk_fma_f32 v[68:69], v[88:89], v[88:89], v[68:69]
	s_nop 0
	v_pk_fma_f32 v[68:69], v[90:91], v[90:91], v[68:69]
	s_nop 0
	v_pk_fma_f32 v[68:69], v[160:161], v[160:161], v[68:69]
	s_nop 0
	v_pk_fma_f32 v[68:69], v[162:163], v[162:163], v[68:69]
	s_nop 0
	v_pk_fma_f32 v[68:69], v[198:199], v[198:199], v[68:69]
	s_nop 0
	v_pk_fma_f32 v[68:69], v[156:157], v[156:157], v[68:69]
	s_nop 0
	v_pk_fma_f32 v[68:69], v[158:159], v[158:159], v[68:69]
	s_nop 0
	v_pk_fma_f32 v[68:69], v[72:73], v[72:73], v[68:69]
	s_nop 0
	v_pk_fma_f32 v[68:69], v[200:201], v[200:201], v[68:69]
	s_nop 0
	v_pk_fma_f32 v[68:69], v[74:75], v[74:75], v[68:69]
	s_nop 1
	v_add_f32_dpp v68, v68, v68 quad_perm:[1,0,3,2] row_mask:0xf bank_mask:0xf
	v_add_f32_dpp v69, v69, v69 quad_perm:[1,0,3,2] row_mask:0xf bank_mask:0xf
	s_nop 1
	v_add_f32_dpp v68, v68, v68 quad_perm:[2,3,0,1] row_mask:0xf bank_mask:0xf
	v_add_f32_dpp v69, v69, v69 quad_perm:[2,3,0,1] row_mask:0xf bank_mask:0xf
	s_nop 1
	v_add_f32_dpp v68, v68, v68 row_half_mirror row_mask:0xf bank_mask:0xf
	v_add_f32_dpp v69, v69, v69 row_half_mirror row_mask:0xf bank_mask:0xf
	s_nop 1
	v_add_f32_dpp v68, v68, v68 row_mirror row_mask:0xf bank_mask:0xf
	v_add_f32_dpp v69, v69, v69 row_mirror row_mask:0xf bank_mask:0xf
	v_mov_b32_e32 v70, v68
	v_mov_b32_e32 v71, v69
	s_nop 1
	v_permlane16_swap_b32_e32 v68, v70
	v_permlane16_swap_b32_e32 v69, v71
	v_add_f32_e32 v68, v68, v70
	v_add_f32_e32 v69, v69, v71
	v_mov_b32_e32 v70, v68
	v_mov_b32_e32 v71, v69
	s_nop 1
	v_permlane32_swap_b32_e32 v68, v70
	v_permlane32_swap_b32_e32 v69, v71
	v_add_f32_e32 v68, v68, v70
	v_add_f32_e32 v69, v69, v71
	s_nop 0
	v_pk_fma_f32 v[68:69], v[68:69], s[0:1], v[196:197] op_sel_hi:[1,0,0]
	s_mov_b32 s0, 0x800000
	v_mul_f32_e32 v1, 0x4b800000, v68
	v_cmp_gt_f32_e32 vcc, s0, v68
	v_cmp_gt_f32_e64 s[0:1], s0, v69
	s_nop 0
	v_cndmask_b32_e32 v1, v68, v1, vcc
	v_rsq_f32_e32 v68, v1
	v_mul_f32_e32 v1, 0x4b800000, v69
	v_cndmask_b32_e64 v1, v69, v1, s[0:1]
	v_rsq_f32_e32 v69, v1
	s_nop 0
	v_pk_mul_f32 v[70:71], v[68:69], s[30:31] op_sel_hi:[1,0]
	s_nop 0
	v_cndmask_b32_e64 v153, v69, v71, s[0:1]
	v_cndmask_b32_e32 v152, v68, v70, vcc
	v_pk_mul_f32 v[68:69], v[184:185], v[152:153]
	v_mov_b32_e32 v70, v5
	v_pk_fma_f32 v[124:125], v[6:7], v[68:69], v[2:3] op_sel_hi:[0,1,0]
	v_pk_mul_f32 v[68:69], v[128:129], v[152:153]
	v_pk_mul_f32 v[74:75], v[74:75], v[152:153]
	v_pk_fma_f32 v[126:127], v[6:7], v[68:69], v[2:3] op_sel:[1,0,1]
	v_pk_mul_f32 v[68:69], v[186:187], v[152:153]
	v_max3_f32 v71, |v125|, 0, |v127|
	v_pk_fma_f32 v[128:129], v[8:9], v[68:69], v[4:5] op_sel_hi:[0,1,0]
	v_pk_mul_f32 v[68:69], v[130:131], v[152:153]
	v_max3_f32 v1, |v124|, 0, |v126|
	v_pk_fma_f32 v[130:131], v[34:35], v[68:69], v[70:71] op_sel_hi:[0,1,0]
	v_pk_mul_f32 v[68:69], v[180:181], v[152:153]
	v_max3_f32 v34, v71, |v129|, |v131|
	v_pk_fma_f32 v[112:113], v[14:15], v[68:69], v[10:11] op_sel_hi:[0,1,0]
	v_pk_mul_f32 v[68:69], v[116:117], v[152:153]
	v_mov_b32_e32 v70, v13
	v_pk_fma_f32 v[114:115], v[14:15], v[68:69], v[10:11] op_sel:[1,0,1]
	v_pk_mul_f32 v[68:69], v[120:121], v[152:153]
	v_max3_f32 v71, v34, |v113|, |v115|
	v_pk_fma_f32 v[118:119], v[16:17], v[68:69], v[12:13] op_sel_hi:[0,1,0]
	v_pk_mul_f32 v[68:69], v[122:123], v[152:153]
	v_mov_b32_e32 v34, v17
	v_pk_fma_f32 v[122:123], v[34:35], v[68:69], v[70:71] op_sel_hi:[0,1,0]
	v_pk_mul_f32 v[68:69], v[176:177], v[152:153]
	v_max3_f32 v34, v71, |v119|, |v123|
	v_pk_fma_f32 v[108:109], v[22:23], v[68:69], v[18:19] op_sel_hi:[0,1,0]
	v_pk_mul_f32 v[68:69], v[178:179], v[152:153]
; __device__ __forceinline__ unsigned pack_i8x4(float a, float b, float c, float d, float inv) { return q8u(a, inv) | (q8u(b, inv) << 8) | (q8u(c, inv) << 16) | (q8u(d, inv) << 24); }
; __device__ __forceinline__ void phase_norm2(const Params& p, const Ctx& F, const int l) {
;     ...
;         f32x2 am = {0.f, 0.f};
; #pragma unroll
;         for (int j = 0; j < 8; ++j)
; #pragma unroll
;             for (int c = 0; c < 4; ++c) { vv[j][c] = vv[j][c] * rstd * A[j][c] + Bv[j][c]; am = __builtin_elementwise_max(am, __builtin_elementwise_abs(vv[j][c])); }
;         const float am0 = fmaxf(wave_max(am.x), 1e-20f), am1 = fmaxf(wave_max(am.y), 1e-20f), inv0 = 127.f / am0, inv1 = 127.f / am1;
;         unsigned* hn0 = (unsigned*)((signed char*)F.r1 + ((size_t)b * TPB + t) * DM) + F.lane;
;         unsigned* hn1 = (unsigned*)((signed char*)F.r1 + ((size_t)b * TPB + (two ? tB : t)) * DM) + F.lane;
; #pragma unroll
;         for (int j = 0; j < 8; ++j) { __builtin_nontemporal_store(pack_i8x4(vv[j][0].x, vv[j][1].x, vv[j][2].x, vv[j][3].x, inv0), hn0 + 64 * j);
;             if (two) __builtin_nontemporal_store(pack_i8x4(vv[j][0].y, vv[j][1].y, vv[j][2].y, vv[j][3].y, inv1), hn1 + 64 * j); }
;         if (F.lane == 0) { F.sah[b * TPB + t] = am0 * (1.f / 127.f); if (two) F.sah[b * TPB + tB] = am1 * (1.f / 127.f); }
	v_mov_b32_e32 v70, v21
	v_pk_fma_f32 v[110:111], v[22:23], v[68:69], v[18:19] op_sel:[1,0,1]
	v_pk_mul_f32 v[68:69], v[182:183], v[152:153]
	v_max3_f32 v71, v34, |v109|, |v111|
	v_pk_fma_f32 v[116:117], v[24:25], v[68:69], v[20:21] op_sel_hi:[0,1,0]
	v_pk_mul_f32 v[68:69], v[172:173], v[152:153]
	v_mov_b32_e32 v34, v25
	v_pk_fma_f32 v[120:121], v[34:35], v[68:69], v[70:71] op_sel_hi:[0,1,0]
	v_pk_mul_f32 v[68:69], v[174:175], v[152:153]
	v_max3_f32 v34, v71, |v117|, |v121|
	v_pk_fma_f32 v[96:97], v[30:31], v[68:69], v[26:27] op_sel_hi:[0,1,0]
	v_pk_mul_f32 v[68:69], v[100:101], v[152:153]
	v_mov_b32_e32 v70, v29
	v_pk_fma_f32 v[98:99], v[30:31], v[68:69], v[26:27] op_sel:[1,0,1]
	v_pk_mul_f32 v[68:69], v[104:105], v[152:153]
	v_max3_f32 v71, v34, |v97|, |v99|
	v_pk_fma_f32 v[102:103], v[32:33], v[68:69], v[28:29] op_sel_hi:[0,1,0]
	v_pk_mul_f32 v[68:69], v[106:107], v[152:153]
	v_mov_b32_e32 v34, v33
	v_pk_fma_f32 v[106:107], v[34:35], v[68:69], v[70:71] op_sel_hi:[0,1,0]
	v_pk_mul_f32 v[68:69], v[164:165], v[152:153]
	v_max3_f32 v1, v1, |v128|, |v130|
	v_pk_fma_f32 v[92:93], v[40:41], v[68:69], v[36:37] op_sel_hi:[0,1,0]
	v_pk_mul_f32 v[68:69], v[168:169], v[152:153]
	v_max3_f32 v1, v1, |v112|, |v114|
	v_max3_f32 v34, v71, |v103|, |v107|
	v_pk_fma_f32 v[94:95], v[40:41], v[68:69], v[36:37] op_sel:[1,0,1]
	v_pk_mul_f32 v[68:69], v[188:189], v[152:153]
	v_max3_f32 v1, v1, |v118|, |v122|
	v_max3_f32 v71, v34, |v93|, |v95|
	v_pk_fma_f32 v[100:101], v[42:43], v[68:69], v[38:39] op_sel_hi:[0,1,0]
	v_pk_mul_f32 v[68:69], v[166:167], v[152:153]
	v_mov_b32_e32 v34, v43
	v_mov_b32_e32 v70, v39
	v_max3_f32 v1, v1, |v108|, |v110|
	v_pk_fma_f32 v[104:105], v[34:35], v[68:69], v[70:71] op_sel_hi:[0,1,0]
	v_pk_mul_f32 v[68:69], v[170:171], v[152:153]
	v_max3_f32 v1, v1, |v116|, |v120|
	v_pk_fma_f32 v[80:81], v[48:49], v[68:69], v[44:45] op_sel_hi:[0,1,0]
	v_pk_mul_f32 v[68:69], v[84:85], v[152:153]
	v_max3_f32 v1, v1, |v96|, |v98|
	v_pk_fma_f32 v[82:83], v[48:49], v[68:69], v[44:45] op_sel:[1,0,1]
	v_pk_mul_f32 v[68:69], v[88:89], v[152:153]
	v_max3_f32 v1, v1, |v102|, |v106|
	v_pk_fma_f32 v[86:87], v[50:51], v[68:69], v[46:47] op_sel_hi:[0,1,0]
	v_pk_mul_f32 v[68:69], v[90:91], v[152:153]
	v_mov_b32_e32 v34, v51
	v_mov_b32_e32 v70, v47
	v_max3_f32 v1, v1, |v92|, |v94|
	v_pk_fma_f32 v[90:91], v[34:35], v[68:69], v[70:71] op_sel_hi:[0,1,0]
	v_pk_mul_f32 v[68:69], v[160:161], v[152:153]
	v_max3_f32 v1, v1, |v100|, |v104|
	v_pk_fma_f32 v[76:77], v[56:57], v[68:69], v[52:53] op_sel_hi:[0,1,0]
	v_pk_mul_f32 v[68:69], v[162:163], v[152:153]
	v_max3_f32 v1, v1, |v80|, |v82|
	v_pk_fma_f32 v[78:79], v[56:57], v[68:69], v[52:53] op_sel:[1,0,1]
	v_pk_mul_f32 v[68:69], v[198:199], v[152:153]
	v_max3_f32 v1, v1, |v86|, |v90|
	v_pk_fma_f32 v[84:85], v[58:59], v[68:69], v[54:55] op_sel_hi:[0,1,0]
	v_pk_mul_f32 v[68:69], v[156:157], v[152:153]
	v_mov_b32_e32 v34, v59
	v_mov_b32_e32 v70, v55
	v_max3_f32 v154, v71, |v101|, |v105|
	v_max3_f32 v1, v1, |v76|, |v78|
	v_pk_fma_f32 v[88:89], v[34:35], v[68:69], v[70:71] op_sel_hi:[0,1,0]
	v_pk_mul_f32 v[68:69], v[158:159], v[152:153]
	v_pk_mul_f32 v[70:71], v[72:73], v[152:153]
	v_max3_f32 v1, v1, |v84|, |v88|
	v_pk_fma_f32 v[68:69], v[60:61], v[68:69], v[64:65] op_sel_hi:[0,1,0]
	v_pk_fma_f32 v[70:71], v[60:61], v[70:71], v[64:65] op_sel:[1,0,1]
	v_pk_mul_f32 v[72:73], v[200:201], v[152:153]
	v_mov_b32_e32 v34, v63
	v_mov_b32_e32 v152, v67
	v_max3_f32 v1, v1, |v68|, |v70|
	v_pk_fma_f32 v[72:73], v[62:63], v[72:73], v[66:67] op_sel_hi:[0,1,0]
	v_pk_fma_f32 v[74:75], v[34:35], v[74:75], v[152:153] op_sel_hi:[0,1,0]
	v_max3_f32 v1, v1, |v72|, |v74|
	ds_bpermute_b32 v34, v133, v1
	v_max3_f32 v152, v154, |v81|, |v83|
	v_max3_f32 v152, v152, |v87|, |v91|
	v_max3_f32 v152, v152, |v77|, |v79|
	v_max3_f32 v152, v152, |v85|, |v89|
	s_waitcnt lgkmcnt(0)
	v_max_f32_e32 v34, v34, v34
	v_max3_f32 v152, v152, |v69|, |v71|
	v_max_f32_e32 v1, v1, v34
	v_max3_f32 v152, v152, |v73|, |v75|
	ds_bpermute_b32 v34, v190, v1
	ds_bpermute_b32 v153, v133, v152
	s_waitcnt lgkmcnt(1)
	v_max_f32_e32 v34, v34, v34
	s_waitcnt lgkmcnt(0)
	v_max_f32_e32 v153, v153, v153
	v_max_f32_e32 v1, v1, v34
	v_max_f32_e32 v152, v152, v153
	ds_bpermute_b32 v34, v191, v1
	ds_bpermute_b32 v153, v190, v152
	s_waitcnt lgkmcnt(1)
	v_max_f32_e32 v34, v34, v34
	s_waitcnt lgkmcnt(0)
	v_max_f32_e32 v153, v153, v153
	v_max_f32_e32 v1, v1, v34
	v_max_f32_e32 v152, v152, v153
	ds_bpermute_b32 v34, v192, v1
	ds_bpermute_b32 v153, v191, v152
	s_waitcnt lgkmcnt(1)
	v_max_f32_e32 v34, v34, v34
	s_waitcnt lgkmcnt(0)
	v_max_f32_e32 v153, v153, v153
	v_max_f32_e32 v1, v1, v34
	v_max_f32_e32 v152, v152, v153
	ds_bpermute_b32 v34, v193, v1
	ds_bpermute_b32 v153, v192, v152
	s_waitcnt lgkmcnt(1)
	v_max_f32_e32 v34, v34, v34
	s_waitcnt lgkmcnt(0)
	v_max_f32_e32 v153, v153, v153
	v_max_f32_e32 v1, v1, v34
	v_max_f32_e32 v152, v152, v153
	ds_bpermute_b32 v34, v194, v1
	ds_bpermute_b32 v153, v193, v152
	s_waitcnt lgkmcnt(1)
	v_max3_f32 v157, v1, v34, s53
	s_waitcnt lgkmcnt(0)
	v_max_f32_e32 v1, v153, v153
	v_max_f32_e32 v1, v152, v1
	ds_bpermute_b32 v34, v194, v1
	v_div_scale_f32 v152, s[0:1], v157, v157, s54
	v_rcp_f32_e32 v153, v152
	s_waitcnt lgkmcnt(0)
	v_max3_f32 v156, v1, v34, s53
	v_fma_f32 v1, -v152, v153, 1.0
	v_fmac_f32_e32 v153, v1, v153
	v_div_scale_f32 v1, vcc, s54, v157, s54
	v_mul_f32_e32 v34, v1, v153
	v_fma_f32 v154, -v152, v34, v1
	v_fmac_f32_e32 v34, v154, v153
	v_fma_f32 v1, -v152, v34, v1
	v_div_scale_f32 v152, s[0:1], v156, v156, s54
	v_rcp_f32_e32 v154, v152
	v_div_fmas_f32 v1, v1, v153, v34
	v_div_fixup_f32 v159, v1, v157, s54
	v_mul_f32_e32 v160, v128, v159
	v_fma_f32 v1, -v152, v154, 1.0
	v_fmac_f32_e32 v154, v1, v154
	v_div_scale_f32 v1, vcc, s54, v156, s54
	v_mul_f32_e32 v34, v1, v154
	v_fma_f32 v153, -v152, v34, v1
	v_fmac_f32_e32 v34, v153, v154
	v_fma_f32 v1, -v152, v34, v1
	v_div_fmas_f32 v1, v1, v154, v34
	v_mul_f32_e32 v34, v126, v159
	v_div_fixup_f32 v158, v1, v156, s54
	v_mul_f32_e32 v1, v124, v159
	v_rndne_f32_e32 v34, v34
	v_rndne_f32_e32 v160, v160
	v_mul_f32_e32 v161, v130, v159
	v_rndne_f32_e32 v1, v1
	v_cvt_i32_f32_e32 v34, v34
	v_cvt_i32_f32_e32 v160, v160
	v_rndne_f32_e32 v161, v161
	v_cvt_i32_f32_e32 v1, v1
	v_cvt_i32_f32_e32 v161, v161
	v_med3_i32 v34, v34, s80, v218
	v_med3_i32 v160, v160, s80, v218
	v_med3_i32 v1, v1, s80, v218
	v_lshlrev_b32_e32 v34, 8, v34
	v_lshlrev_b32_e32 v160, 16, v160
	v_med3_i32 v161, v161, s80, v218
	v_and_b32_e32 v34, 0xff00, v34
	v_and_b32_e32 v160, 0xff0000, v160
	v_perm_b32 v1, v161, v1, s81
	v_or3_b32 v1, v1, v34, v160
	v_cndmask_b32_e64 v34, 0, 1, s[8:9]
	v_lshl_add_u64 v[154:155], v[136:137], 0, s[12:13]
	v_lshl_add_u64 v[152:153], v[136:137], 0, s[14:15]
	v_cmp_ne_u32_e64 s[0:1], 1, v34
	s_andn2_b64 vcc, exec, s[8:9]
	global_store_dword v[154:155], v1, off nt
	s_cbranch_vccnz .LBB0_920
; __device__ __forceinline__ unsigned pack_i8x4(float a, float b, float c, float d, float inv) { return q8u(a, inv) | (q8u(b, inv) << 8) | (q8u(c, inv) << 16) | (q8u(d, inv) << 24); }
; __device__ __forceinline__ void phase_norm2(const Params& p, const Ctx& F, const int l) {
;     ...
;         for (int j = 0; j < 8; ++j) { __builtin_nontemporal_store(pack_i8x4(vv[j][0].x, vv[j][1].x, vv[j][2].x, vv[j][3].x, inv0), hn0 + 64 * j);
;             if (two) __builtin_nontemporal_store(pack_i8x4(vv[j][0].y, vv[j][1].y, vv[j][2].y, vv[j][3].y, inv1), hn1 + 64 * j); }
;         if (F.lane == 0) { F.sah[b * TPB + t] = am0 * (1.f / 127.f); if (two) F.sah[b * TPB + tB] = am1 * (1.f / 127.f); }
	v_mul_f32_e32 v160, v127, v158
	v_mul_f32_e32 v161, v129, v158
	v_mul_f32_e32 v1, v125, v158
	v_rndne_f32_e32 v160, v160
	v_rndne_f32_e32 v161, v161
	v_mul_f32_e32 v162, v131, v158
	v_rndne_f32_e32 v1, v1
	v_cvt_i32_f32_e32 v160, v160
	v_cvt_i32_f32_e32 v161, v161
	v_rndne_f32_e32 v162, v162
	v_cvt_i32_f32_e32 v1, v1
	v_cvt_i32_f32_e32 v162, v162
	v_med3_i32 v160, v160, s80, v218
	v_med3_i32 v161, v161, s80, v218
	v_med3_i32 v1, v1, s80, v218
	v_lshlrev_b32_e32 v160, 8, v160
	v_lshlrev_b32_e32 v161, 16, v161
	v_med3_i32 v162, v162, s80, v218
	v_and_b32_e32 v160, 0xff00, v160
	v_and_b32_e32 v161, 0xff0000, v161
	v_perm_b32 v1, v162, v1, s81
	v_or3_b32 v1, v1, v160, v161
	global_store_dword v[152:153], v1, off nt

; __device__ __forceinline__ float bflo(unsigned w) { return __uint_as_float(w << 16); }
; __device__ __forceinline__ float bfhi(unsigned w) { return __uint_as_float(w & 0xffff0000u); }
; __device__ __forceinline__ void phase_norm1(const Params& p, const Ctx& F, const int l) {
;     ...
;         for (int j = 0; j < 8; ++j) v[j] = vn[j] + (f32x4){bflo(dn[j].x), bfhi(dn[j].x), bflo(dn[j].y), bfhi(dn[j].y)};
;         if (comb) {
;             const float* gt = F.mod + (size_t)((l - 1) * 9 + mrow) * MODW + 5 * DM;
; #pragma unroll
;             for (int j = 0; j < 8; ++j) { v[j] += *((const f32x4*)gt + F.lane + 64 * j) * accn[j] * (1.f / Y_SCALE); if (!fin) *((f32x4*)xd + F.lane + 64 * j) = v[j]; }
;         }
;         { const int t2 = t + tstride;
;           if (t2 < TPB) { const float* xs2; float* xd2; row_ptrs(p, F, l, b, t2, xs2, xd2);
; #pragma unroll
;             for (int j = 0; j < 8; ++j) vn[j] = __builtin_nontemporal_load((const f32x4*)xs2 + F.lane + 64 * j);
;             if (comb) {
; #pragma unroll
;                 for (int j = 0; j < 8; ++j) dn[j] = __builtin_nontemporal_load((const u32x2*)(F.dlt + ((size_t)b * TPB + t2) * DM + 4 * F.lane + 256 * j)); }
;             if (comb) { { if (fin) gather_y1(F, sn, accn); else gather_y(F, sn, accn); } const int t3 = t2 + tstride; sn = -1; if (t3 < TPB && F.lane < 16) sn = F.slot[(unsigned)((b * 16 + F.lane) * TPB + t3)]; } } }
;         if (mrow != cur_m) { cur_m = mrow;
;             if (!fin) {
;                 const float* mr = F.mod + (size_t)(l * 9 + mrow) * MODW;
; #pragma unroll
;                 for (int j = 0; j < 8; ++j) { const f32x4 g = *((const f32x4*)(p.g_mix + l * DM) + F.lane + 64 * j), sc = *((const f32x4*)(mr + DM) + F.lane + 64 * j);
;                     A[j] = g * (sc + 1.f); Bv[j] = *((const f32x4*)mr + F.lane + 64 * j); }
;             }
;         }
;         float ss = 0.f;
; #pragma unroll
;         for (int j = 0; j < 8; ++j) ss += (v[j].x * v[j].x + v[j].y * v[j].y) + (v[j].z * v[j].z + v[j].w * v[j].w);
;         const float rstd = rsqrtf(wave_sum(ss) * (1.f / DM) + EPS);
.LBB0_1459:
	v_lshlrev_b32_e32 v96, 16, v146
	v_and_b32_e32 v97, 0xffff0000, v146
	v_lshlrev_b32_e32 v98, 16, v147
	v_and_b32_e32 v99, 0xffff0000, v147
	v_pk_add_f32 v[28:29], v[28:29], v[96:97]
	v_pk_add_f32 v[30:31], v[30:31], v[98:99]
	v_lshlrev_b32_e32 v96, 16, v144
	v_and_b32_e32 v97, 0xffff0000, v144
	v_lshlrev_b32_e32 v98, 16, v145
	v_and_b32_e32 v99, 0xffff0000, v145
	v_pk_add_f32 v[24:25], v[24:25], v[96:97]
	v_pk_add_f32 v[26:27], v[26:27], v[98:99]
	v_lshlrev_b32_e32 v96, 16, v142
	v_and_b32_e32 v97, 0xffff0000, v142
	v_lshlrev_b32_e32 v98, 16, v143
	v_and_b32_e32 v99, 0xffff0000, v143
	v_pk_add_f32 v[20:21], v[20:21], v[96:97]
	v_pk_add_f32 v[22:23], v[22:23], v[98:99]
	v_lshlrev_b32_e32 v96, 16, v140
	v_and_b32_e32 v97, 0xffff0000, v140
	v_lshlrev_b32_e32 v98, 16, v141
	v_and_b32_e32 v99, 0xffff0000, v141
	v_pk_add_f32 v[16:17], v[16:17], v[96:97]
	v_pk_add_f32 v[18:19], v[18:19], v[98:99]
	v_lshlrev_b32_e32 v96, 16, v138
	v_and_b32_e32 v97, 0xffff0000, v138
	v_lshlrev_b32_e32 v98, 16, v139
	v_and_b32_e32 v99, 0xffff0000, v139
	v_pk_add_f32 v[12:13], v[12:13], v[96:97]
	v_pk_add_f32 v[14:15], v[14:15], v[98:99]
	v_lshlrev_b32_e32 v96, 16, v136
	v_and_b32_e32 v97, 0xffff0000, v136
	v_lshlrev_b32_e32 v98, 16, v137
	v_and_b32_e32 v99, 0xffff0000, v137
	v_pk_add_f32 v[96:97], v[8:9], v[96:97]
	v_pk_add_f32 v[8:9], v[10:11], v[98:99]
	v_lshlrev_b32_e32 v10, 16, v134
	v_and_b32_e32 v11, 0xffff0000, v134
	v_lshlrev_b32_e32 v98, 16, v135
	v_and_b32_e32 v99, 0xffff0000, v135
	v_pk_add_f32 v[100:101], v[4:5], v[10:11]
	v_lshlrev_b32_e32 v4, 16, v132
	v_and_b32_e32 v5, 0xffff0000, v132
	v_pk_add_f32 v[98:99], v[6:7], v[98:99]
	v_lshlrev_b32_e32 v6, 16, v133
	v_and_b32_e32 v7, 0xffff0000, v133
	v_pk_add_f32 v[102:103], v[0:1], v[4:5]
	s_waitcnt vmcnt(5)
	v_pk_mul_f32 v[0:1], v[154:155], v[94:95]
	v_pk_add_f32 v[104:105], v[2:3], v[6:7]
	v_pk_mul_f32 v[2:3], v[148:149], v[92:93]
	v_pk_fma_f32 v[30:31], v[0:1], s[12:13], v[30:31] op_sel_hi:[1,0,1]
	v_pk_mul_f32 v[0:1], v[156:157], v[90:91]
	v_pk_fma_f32 v[28:29], v[2:3], s[12:13], v[28:29] op_sel_hi:[1,0,1]
	v_pk_mul_f32 v[2:3], v[150:151], v[88:89]
	v_pk_fma_f32 v[26:27], v[0:1], s[12:13], v[26:27] op_sel_hi:[1,0,1]
	v_pk_mul_f32 v[0:1], v[160:161], v[86:87]
	v_pk_fma_f32 v[24:25], v[2:3], s[12:13], v[24:25] op_sel_hi:[1,0,1]
	v_pk_mul_f32 v[2:3], v[152:153], v[84:85]
	v_pk_fma_f32 v[22:23], v[0:1], s[12:13], v[22:23] op_sel_hi:[1,0,1]
	s_waitcnt vmcnt(4)
	v_pk_mul_f32 v[0:1], v[164:165], v[82:83]
	v_pk_fma_f32 v[20:21], v[2:3], s[12:13], v[20:21] op_sel_hi:[1,0,1]
	v_pk_mul_f32 v[2:3], v[158:159], v[80:81]
	v_pk_fma_f32 v[18:19], v[0:1], s[12:13], v[18:19] op_sel_hi:[1,0,1]
	s_waitcnt vmcnt(3)
	v_pk_mul_f32 v[0:1], v[168:169], v[78:79]
	v_pk_fma_f32 v[16:17], v[2:3], s[12:13], v[16:17] op_sel_hi:[1,0,1]
	v_pk_mul_f32 v[2:3], v[162:163], v[76:77]
	v_pk_fma_f32 v[4:5], v[0:1], s[12:13], v[14:15] op_sel_hi:[1,0,1]
	s_waitcnt vmcnt(0)
	s_add_i32 s6, s26, s13
	s_cmpk_lt_i32 s6, 0x1100
	s_cselect_b64 s[24:25], -1, 0
	s_and_b64 s[24:25], s[24:25], s[0:1]
	v_cndmask_b32_e64 v208, -1, v250, s[24:25]
	v_pk_mul_f32 v[14:15], v[174:175], v[64:65]
	v_pk_fma_f32 v[6:7], v[2:3], s[12:13], v[12:13] op_sel_hi:[1,0,1]
	v_pk_mul_f32 v[2:3], v[166:167], v[72:73]
	v_pk_mul_f32 v[12:13], v[178:179], v[66:67]
	v_pk_fma_f32 v[66:67], v[14:15], s[12:13], v[102:103] op_sel_hi:[1,0,1]
	v_mov_b32_e32 v14, v29
	v_mov_b32_e32 v15, v25
	v_pk_fma_f32 v[10:11], v[2:3], s[12:13], v[96:97] op_sel_hi:[1,0,1]
	v_pk_mul_f32 v[2:3], v[170:171], v[68:69]
	v_pk_fma_f32 v[64:65], v[12:13], s[12:13], v[104:105] op_sel_hi:[1,0,1]
	v_mov_b32_e32 v12, v28
	v_mov_b32_e32 v13, v24
	v_pk_mul_f32 v[14:15], v[14:15], v[14:15]
	v_mov_b32_e32 v68, v31
	v_mov_b32_e32 v69, v27
	v_pk_fma_f32 v[12:13], v[12:13], v[12:13], v[14:15]
	v_mov_b32_e32 v14, v30
	v_mov_b32_e32 v15, v26
	v_pk_mul_f32 v[68:69], v[68:69], v[68:69]
	v_pk_mul_f32 v[0:1], v[172:173], v[74:75]
	v_pk_fma_f32 v[14:15], v[14:15], v[14:15], v[68:69]
	v_pk_mul_f32 v[68:69], v[20:21], v[20:21]
	v_pk_add_f32 v[12:13], v[12:13], v[14:15]
	v_pk_mul_f32 v[14:15], v[22:23], v[22:23]
	v_pk_fma_f32 v[8:9], v[0:1], s[12:13], v[8:9] op_sel_hi:[1,0,1]
	v_pk_mul_f32 v[0:1], v[176:177], v[70:71]
	v_pk_mov_b32 v[70:71], v[68:69], v[14:15] op_sel:[1,0]
	v_mov_b32_e32 v69, v15
	v_pk_add_f32 v[14:15], v[70:71], v[68:69]
	v_mul_f32_e32 v68, v6, v6
	v_mul_f32_e32 v69, v7, v7
	v_pk_add_f32 v[12:13], v[12:13], v[12:13] op_sel:[0,1] op_sel_hi:[1,0]
	v_pk_add_f32 v[14:15], v[14:15], v[14:15] op_sel:[0,1] op_sel_hi:[1,0]
	v_mov_b32_e32 v13, v68
	v_mov_b32_e32 v15, v69
	v_pk_add_f32 v[68:69], v[12:13], v[14:15]
	global_load_dwordx4 v[12:15], v[180:181], off
	global_load_dwordx4 v[76:79], v[180:181], off offset:1024
	global_load_dwordx4 v[80:83], v[180:181], off offset:2048
	global_load_dwordx4 v[84:87], v[180:181], off offset:3072
	global_load_dwordx4 v[88:91], v[182:183], off
	global_load_dwordx4 v[92:95], v[184:185], off
	global_load_dwordx4 v[108:111], v[186:187], off
	global_load_dwordx4 v[112:115], v[188:189], off
	v_mul_f32_e32 v70, v17, v17
	v_mul_f32_e32 v72, v4, v4
	v_pk_fma_f32 v[70:71], v[16:17], v[16:17], v[70:71] op_sel_hi:[1,1,0]
	v_mul_f32_e32 v74, v5, v5
	v_mov_b32_e32 v71, v72
	v_mul_f32_e32 v72, v19, v19
	v_pk_fma_f32 v[72:73], v[18:19], v[18:19], v[72:73] op_sel_hi:[1,1,0]
	v_pk_fma_f32 v[0:1], v[0:1], s[12:13], v[98:99] op_sel_hi:[1,0,1]
	v_mov_b32_e32 v73, v74
	v_pk_add_f32 v[70:71], v[70:71], v[72:73]
	v_pk_mul_f32 v[72:73], v[10:11], v[10:11]
	v_pk_add_f32 v[68:69], v[68:69], v[70:71]
	v_pk_mul_f32 v[70:71], v[8:9], v[8:9]
	v_pk_add_f32 v[68:69], v[68:69], v[68:69] op_sel:[0,1] op_sel_hi:[1,0]
; __device__ __forceinline__ float wave_sum(float v) {
; #pragma unroll
;     for (int o = 1; o < 64; o <<= 1) v += __shfl_xor(v, o);
;     return v;
; __device__ __forceinline__ void phase_norm1(const Params& p, const Ctx& F, const int l) {
;     ...
;         float ss = 0.f;
; #pragma unroll
;         for (int j = 0; j < 8; ++j) ss += (v[j].x * v[j].x + v[j].y * v[j].y) + (v[j].z * v[j].z + v[j].w * v[j].w);
;         const float rstd = rsqrtf(wave_sum(ss) * (1.f / DM) + EPS);
;         if (fin) {
; #pragma unroll
;             for (int j = 0; j < 8; ++j) __builtin_nontemporal_store(v[j] * rstd * *((const f32x4*)p.g_final + F.lane + 64 * j), (f32x4*)xd + F.lane + 64 * j);
	v_pk_mov_b32 v[74:75], v[72:73], v[70:71] op_sel:[1,0]
	v_mov_b32_e32 v73, v71
	v_pk_add_f32 v[70:71], v[74:75], v[72:73]
	v_mul_f32_e32 v72, v66, v66
	v_mul_f32_e32 v73, v67, v67
	v_pk_add_f32 v[70:71], v[70:71], v[70:71] op_sel:[0,1] op_sel_hi:[1,0]
	v_pk_fma_f32 v[2:3], v[2:3], s[12:13], v[100:101] op_sel_hi:[1,0,1]
	v_mov_b32_e32 v69, v72
	v_mov_b32_e32 v71, v73
	v_pk_add_f32 v[68:69], v[68:69], v[70:71]
	v_mul_f32_e32 v70, v3, v3
	v_mul_f32_e32 v72, v1, v1
	v_mul_f32_e32 v74, v64, v64
	v_mul_f32_e32 v75, v65, v65
	v_pk_fma_f32 v[70:71], v[2:3], v[2:3], v[70:71] op_sel_hi:[1,1,0]
	v_pk_fma_f32 v[72:73], v[0:1], v[0:1], v[72:73] op_sel_hi:[1,1,0]
	v_mov_b32_e32 v71, v74
	v_mov_b32_e32 v73, v75
	v_pk_add_f32 v[70:71], v[70:71], v[72:73]
	s_lshl_b64 s[16:17], s[16:17], 13
	v_pk_add_f32 v[68:69], v[68:69], v[70:71]
	s_add_u32 s16, s18, s16
	v_add_f32_e32 v68, v68, v69
	s_addc_u32 s17, s19, s17
	v_mov_b64_e32 v[132:133], v[206:207]
	v_mov_b64_e32 v[134:135], v[204:205]
	v_mov_b64_e32 v[136:137], v[202:203]
	s_nop 1
	v_add_f32_dpp v68, v68, v68 quad_perm:[1,0,3,2] row_mask:0xf bank_mask:0xf
	v_mov_b64_e32 v[138:139], v[200:201]
	v_mov_b64_e32 v[140:141], v[198:199]
	v_mov_b64_e32 v[142:143], v[196:197]
	v_mov_b64_e32 v[144:145], v[194:195]
	s_nop 1
	v_add_f32_dpp v68, v68, v68 quad_perm:[2,3,0,1] row_mask:0xf bank_mask:0xf
	v_mov_b64_e32 v[146:147], v[192:193]
	v_mov_b32_e32 v148, v217
	v_mov_b32_e32 v149, v218
	v_mov_b32_e32 v154, v219
	s_nop 1
	v_add_f32_dpp v68, v68, v68 row_half_mirror row_mask:0xf bank_mask:0xf
	v_mov_b32_e32 v155, v220
	v_mov_b32_e32 v150, v221
	v_mov_b32_e32 v151, v222
	v_mov_b32_e32 v156, v223
	s_nop 1
	v_add_f32_dpp v68, v68, v68 row_mirror row_mask:0xf bank_mask:0xf
	v_mov_b32_e32 v157, v224
	v_mov_b32_e32 v152, v225
	v_mov_b32_e32 v153, v226
	v_mov_b32_e32 v160, v227
	v_mov_b32_e32 v69, v68
	s_nop 1
	v_permlane16_swap_b32_e32 v68, v69
	v_add_f32_e32 v68, v68, v69
	v_mov_b32_e32 v161, v228
	v_mov_b32_e32 v158, v229
	v_mov_b32_e32 v159, v230
	v_mov_b32_e32 v164, v231
	v_mov_b32_e32 v69, v68
	s_nop 1
	v_permlane32_swap_b32_e32 v68, v69
	v_add_f32_e32 v68, v68, v69
	v_fmamk_f32 v68, v68, 0x3a000000, v216
	v_mul_f32_e32 v69, 0x4b800000, v68
	v_cmp_gt_f32_e32 vcc, s31, v68
	v_mov_b32_e32 v165, v232
	v_mov_b32_e32 v162, v233
	v_cndmask_b32_e32 v68, v68, v69, vcc
	v_rsq_f32_e32 v68, v68
	v_mov_b32_e32 v163, v235
	v_mov_b32_e32 v168, v236
	v_mov_b32_e32 v169, v237
	v_mul_f32_e32 v69, 0x45800000, v68
	v_cndmask_b32_e32 v72, v68, v69, vcc
	v_pk_mul_f32 v[28:29], v[28:29], v[72:73] op_sel_hi:[1,0]
	v_pk_mul_f32 v[30:31], v[30:31], v[72:73] op_sel_hi:[1,0]
	s_waitcnt vmcnt(0)
	v_pk_mul_f32 v[12:13], v[12:13], v[28:29]
	v_pk_mul_f32 v[14:15], v[14:15], v[30:31]
	global_store_dwordx4 v128, v[12:15], s[16:17] nt
	v_pk_mul_f32 v[26:27], v[26:27], v[72:73] op_sel_hi:[1,0]
	v_pk_mul_f32 v[24:25], v[24:25], v[72:73] op_sel_hi:[1,0]
	v_pk_mul_f32 v[22:23], v[22:23], v[72:73] op_sel_hi:[1,0]
	v_pk_mul_f32 v[20:21], v[20:21], v[72:73] op_sel_hi:[1,0]
	v_pk_mul_f32 v[18:19], v[18:19], v[72:73] op_sel_hi:[1,0]
	v_pk_mul_f32 v[16:17], v[16:17], v[72:73] op_sel_hi:[1,0]
	v_pk_mul_f32 v[8:9], v[8:9], v[72:73] op_sel_hi:[1,0]
	v_pk_mul_f32 v[10:11], v[10:11], v[72:73] op_sel_hi:[1,0]
	v_mov_b64_e32 v[28:29], v[32:33]
	v_mov_b64_e32 v[30:31], v[34:35]
	v_pk_mul_f32 v[34:35], v[64:65], v[72:73] op_sel_hi:[1,0]
	v_pk_mul_f32 v[32:33], v[66:67], v[72:73] op_sel_hi:[1,0]
	v_mov_b32_e32 v166, v238
	v_mov_b32_e32 v167, v239
	v_mov_b32_e32 v172, v240
	v_mov_b32_e32 v173, v241
	v_mov_b32_e32 v170, v242
	v_mov_b32_e32 v171, v243
	v_mov_b32_e32 v176, v244
	v_mov_b32_e32 v177, v245
	v_mov_b32_e32 v174, v246
	v_mov_b32_e32 v175, v247
	v_mov_b32_e32 v178, v248
	v_mov_b32_e32 v179, v234
	v_pk_mul_f32 v[76:77], v[76:77], v[24:25]
	v_pk_mul_f32 v[78:79], v[78:79], v[26:27]
	global_store_dwordx4 v128, v[76:79], s[16:17] offset:1024 nt
	v_mov_b64_e32 v[24:25], v[36:37]
	v_mov_b64_e32 v[26:27], v[38:39]
	v_pk_mul_f32 v[80:81], v[80:81], v[20:21]
	v_pk_mul_f32 v[82:83], v[82:83], v[22:23]
	global_store_dwordx4 v128, v[80:83], s[16:17] offset:2048 nt
	v_mov_b64_e32 v[20:21], v[40:41]
	v_mov_b64_e32 v[22:23], v[42:43]
	v_pk_mul_f32 v[84:85], v[84:85], v[16:17]
	v_pk_mul_f32 v[86:87], v[86:87], v[18:19]
	global_store_dwordx4 v128, v[84:87], s[16:17] offset:3072 nt
	v_lshl_add_u64 v[16:17], s[16:17], 0, v[128:129]
	v_add_co_u32_e32 v74, vcc, s30, v16
	s_nop 1
	v_addc_co_u32_e32 v75, vcc, 0, v17, vcc
	v_pk_mul_f32 v[16:17], v[4:5], v[72:73] op_sel_hi:[1,0]
	v_pk_mul_f32 v[4:5], v[6:7], v[72:73] op_sel_hi:[1,0]
	s_andn2_b64 vcc, exec, s[14:15]
	v_pk_mul_f32 v[4:5], v[88:89], v[4:5]
	v_pk_mul_f32 v[6:7], v[90:91], v[16:17]
	global_store_dwordx4 v[74:75], v[4:7], off nt
	v_mov_b64_e32 v[12:13], v[48:49]
	v_mov_b64_e32 v[16:17], v[44:45]
	v_mov_b64_e32 v[14:15], v[50:51]
	v_mov_b64_e32 v[18:19], v[46:47]
	v_pk_mul_f32 v[4:5], v[92:93], v[10:11]
	v_pk_mul_f32 v[6:7], v[94:95], v[8:9]
	global_store_dwordx4 v[74:75], v[4:7], off offset:1024 nt
	v_pk_mul_f32 v[8:9], v[0:1], v[72:73] op_sel_hi:[1,0]
	v_pk_mul_f32 v[0:1], v[2:3], v[72:73] op_sel_hi:[1,0]
	v_pk_mul_f32 v[2:3], v[8:9], v[110:111]
	v_pk_mul_f32 v[0:1], v[0:1], v[108:109]
	global_store_dwordx4 v[74:75], v[0:3], off offset:2048 nt
	s_nop 1
	v_mov_b64_e32 v[4:5], v[56:57]
	v_mov_b64_e32 v[0:1], v[60:61]
	v_mov_b64_e32 v[8:9], v[52:53]
	v_mov_b64_e32 v[2:3], v[62:63]
	v_mov_b64_e32 v[6:7], v[58:59]
	v_mov_b64_e32 v[10:11], v[54:55]
	v_pk_mul_f32 v[32:33], v[32:33], v[112:113]
	v_pk_mul_f32 v[34:35], v[34:35], v[114:115]
	global_store_dwordx4 v[74:75], v[32:35], off offset:3072 nt
	s_cbranch_vccz .LBB0_1478
